# speedup vs baseline: 1.0260x; 1.0260x over previous
.LBB8_4:
	s_load_dwordx4 s[32:35], s[0:1], 0x18
	s_load_dword s36, s[0:1], 0x28
	s_load_dwordx4 s[4:7], s[0:1], 0x60
	s_load_dwordx2 s[14:15], s[0:1], 0x10
	s_ashr_i32 s2, s2, 3
	s_add_i32 s2, s3, s2
	s_abs_i32 s3, s2
	s_waitcnt lgkmcnt(0)
	s_abs_i32 s16, s6
	v_cvt_f32_u32_e32 v2, s16
	s_sub_i32 s18, 0, s16
	s_xor_b32 s17, s2, s6
	s_ashr_i32 s17, s17, 31
	v_rcp_iflag_f32_e32 v2, v2
	v_lshrrev_b32_e32 v1, 6, v0
	v_lshrrev_b32_e32 v3, 2, v0
	v_mov_b32_e32 v17, 0
	v_mul_f32_e32 v2, 0x4f7ffffe, v2
	v_cvt_u32_f32_e32 v2, v2
	v_and_b32_e32 v12, 31, v0
	v_accvgpr_write_b32 a0, 0
	v_accvgpr_write_b32 a1, 0
	v_readfirstlane_b32 s19, v2
	s_mul_i32 s18, s18, s19
	s_mul_hi_u32 s18, s19, s18
	s_add_i32 s19, s19, s18
	s_mul_hi_u32 s18, s3, s19
	s_mul_i32 s19, s18, s16
	s_sub_i32 s3, s3, s19
	s_add_i32 s20, s18, 1
	s_sub_i32 s19, s3, s16
	s_cmp_ge_u32 s3, s16
	s_cselect_b32 s18, s20, s18
	s_cselect_b32 s3, s19, s3
	s_add_i32 s19, s18, 1
	s_cmp_ge_u32 s3, s16
	s_cselect_b32 s3, s19, s18
	s_abs_i32 s16, s7
	v_cvt_f32_u32_e32 v2, s16
	s_xor_b32 s3, s3, s17
	s_sub_i32 s3, s3, s17
	s_mul_i32 s6, s3, s6
	v_rcp_iflag_f32_e32 v2, v2
	s_sub_i32 s19, 0, s16
	s_sub_i32 s18, s2, s6
	s_xor_b32 s17, s3, s7
	v_mul_f32_e32 v2, 0x4f7ffffe, v2
	v_cvt_u32_f32_e32 v2, v2
	s_ashr_i32 s2, s17, 31
	s_abs_i32 s20, s3
	v_accvgpr_write_b32 a2, 0
	v_readfirstlane_b32 s6, v2
	s_mul_i32 s19, s19, s6
	s_mul_hi_u32 s17, s6, s19
	s_add_i32 s6, s6, s17
	s_mul_hi_u32 s6, s20, s6
	s_mul_i32 s17, s6, s16
	s_sub_i32 s17, s20, s17
	s_add_i32 s19, s6, 1
	s_sub_i32 s20, s17, s16
	s_cmp_ge_u32 s17, s16
	s_cselect_b32 s6, s19, s6
	s_cselect_b32 s17, s20, s17
	s_add_i32 s19, s6, 1
	s_cmp_ge_u32 s17, s16
	s_cselect_b32 s6, s19, s6
	s_xor_b32 s6, s6, s2
	s_sub_i32 s2, s6, s2
	s_mul_i32 s6, s2, s7
	s_sub_i32 s3, s3, s6
	v_lshlrev_b32_e32 v2, 3, v0
	s_mul_i32 s6, s2, s4
	s_lshl_b32 s16, s3, 6
	v_and_b32_e32 v16, 24, v2
	s_ashr_i32 s7, s6, 31
	v_or_b32_e32 v6, s16, v3
	s_ashr_i32 s17, s16, 31
	v_lshl_add_u64 v[4:5], s[6:7], 0, v[16:17]
	v_lshlrev_b32_e32 v2, 5, v1
	v_lshl_or_b32 v2, s18, 7, v2
	s_mul_i32 s19, s14, s17
	v_mad_u64_u32 v[4:5], s[2:3], s14, v6, v[4:5]
	v_mul_lo_u32 v6, s15, v6
	v_add3_u32 v5, v6, v5, s19
	v_or_b32_e32 v14, v2, v12
	v_lshlrev_b64 v[6:7], 1, v[4:5]
	v_ashrrev_i32_e32 v15, 31, v14
	v_lshl_add_u64 v[4:5], s[10:11], 0, v[6:7]
	v_lshl_add_u64 v[6:7], s[8:9], 0, v[6:7]
	v_lshl_add_u64 v[14:15], v[14:15], 2, s[12:13]
	global_load_dwordx4 v[78:81], v[6:7], off
	global_load_dwordx4 v[82:85], v[4:5], off
	global_load_dword v13, v[14:15], off
	s_load_dwordx2 s[2:3], s[0:1], 0x38
	s_movk_i32 s9, 0x50
	v_lshlrev_b32_e32 v16, 1, v16
	v_and_b32_e32 v14, 63, v0
	v_accvgpr_write_b32 a3, 0
	v_accvgpr_write_b32 a4, 0
	v_accvgpr_write_b32 a5, 0
	v_accvgpr_write_b32 a6, 0
	v_accvgpr_write_b32 a7, 0
	v_accvgpr_write_b32 a8, 0
	v_accvgpr_write_b32 a9, 0
	v_accvgpr_write_b32 a10, 0
	v_accvgpr_write_b32 a11, 0
	v_accvgpr_write_b32 a12, 0
	v_accvgpr_write_b32 a13, 0
	v_accvgpr_write_b32 a14, 0
	v_accvgpr_write_b32 a15, 0
	v_accvgpr_write_b32 a16, 0
	v_accvgpr_write_b32 a17, 0
	v_accvgpr_write_b32 a18, 0
	v_accvgpr_write_b32 a19, 0
	v_accvgpr_write_b32 a20, 0
	v_accvgpr_write_b32 a21, 0
	v_accvgpr_write_b32 a22, 0
	v_accvgpr_write_b32 a23, 0
	v_accvgpr_write_b32 a24, 0
	v_accvgpr_write_b32 a25, 0
	v_accvgpr_write_b32 a26, 0
	v_accvgpr_write_b32 a27, 0
	v_accvgpr_write_b32 a28, 0
	v_accvgpr_write_b32 a29, 0
	v_accvgpr_write_b32 a30, 0
	v_accvgpr_write_b32 a31, 0
	v_bfe_u32 v15, v0, 5, 1
	v_mad_u32_u24 v17, v3, s9, v16
	s_mov_b32 s10, s36
	s_lshr_b32 s7, s7, 28
	v_lshl_or_b32 v10, s18, 2, v1
	s_add_i32 s6, s6, s7
	s_ashr_i32 s6, s6, 4
	s_waitcnt lgkmcnt(0)
	s_ashr_i32 s18, s10, 31
	s_lshr_b32 s18, s18, 28
	s_ashr_i32 s8, s4, 31
	s_add_i32 s10, s10, s18
	s_ashr_i32 s7, s6, 31
	s_lshr_b32 s8, s8, 27
	s_ashr_i32 s10, s10, 4
	v_mov_b32_e32 v8, s6
	v_mov_b32_e32 v9, s7
	s_add_i32 s4, s4, s8
	v_mad_i64_i32 v[8:9], s[6:7], v10, s10, v[8:9]
	s_ashr_i32 s4, s4, 5
	v_lshlrev_b64 v[10:11], 10, v[8:9]
	s_add_i32 s8, s4, -1
	v_lshl_or_b32 v10, v14, 4, v10
	s_min_i32 s11, s8, 2
	v_lshl_add_u64 v[8:9], s[32:33], 0, v[10:11]
	global_load_dwordx4 v[30:33], v[6:7], off offset:64
	global_load_dwordx4 v[22:25], v[4:5], off offset:64
	v_lshl_add_u64 v[10:11], s[34:35], 0, v[10:11]
	global_load_dwordx4 v[38:41], v[8:9], off
	global_load_dwordx4 v[18:21], v[8:9], off offset:1024
	global_load_dwordx4 v[54:57], v[10:11], off
	global_load_dwordx4 v[26:29], v[10:11], off offset:1024
	global_load_dwordx4 v[42:45], v[8:9], off offset:2048
	global_load_dwordx4 v[50:53], v[10:11], off offset:2048
	s_lshl_b32 s6, s11, 5
	s_ashr_i32 s7, s6, 31
	s_lshl_b64 s[6:7], s[6:7], 1
	v_lshl_add_u64 v[60:61], v[6:7], 0, s[6:7]
	v_lshl_add_u64 v[58:59], v[4:5], 0, s[6:7]
	global_load_dwordx4 v[46:49], v[60:61], off
	global_load_dwordx4 v[34:37], v[58:59], off
	s_waitcnt vmcnt(12)
	ds_write_b128 v17, v[78:81]
	s_waitcnt vmcnt(11)
	ds_write_b128 v17, v[82:85] offset:5120
	s_waitcnt lgkmcnt(0)
	s_barrier
	v_mul_u32_u24_e32 v17, 0x50, v3
	v_lshlrev_b32_e32 v3, 4, v15
	v_mad_u32_u24 v70, v12, s9, v3
	ds_read_b128 v[58:61], v70 offset:2560
	ds_read_b128 v[66:69], v70
	ds_read_b128 v[62:65], v70 offset:7680
	ds_read_b128 v[70:73], v70 offset:5120
	v_mul_u32_u24_e32 v74, 0x50, v12
	s_mov_b32 s6, 4
	v_accvgpr_write_b32 a31, 0
	v_accvgpr_write_b32 a30, 0
	v_accvgpr_write_b32 a29, 0
	v_accvgpr_write_b32 a28, 0
	v_accvgpr_write_b32 a27, 0
	v_accvgpr_write_b32 a26, 0
	v_accvgpr_write_b32 a25, 0
	v_accvgpr_write_b32 a24, 0
	v_accvgpr_write_b32 a23, 0
	v_accvgpr_write_b32 a22, 0
	v_accvgpr_write_b32 a21, 0
	v_accvgpr_write_b32 a20, 0
	v_accvgpr_write_b32 a19, 0
	v_accvgpr_write_b32 a18, 0
	v_accvgpr_write_b32 a17, 0
	v_accvgpr_write_b32 a16, 0
	v_accvgpr_write_b32 a15, 0
	v_accvgpr_write_b32 a14, 0
	v_accvgpr_write_b32 a13, 0
	v_accvgpr_write_b32 a12, 0
	v_accvgpr_write_b32 a11, 0
	v_accvgpr_write_b32 a10, 0
	v_accvgpr_write_b32 a9, 0
	v_accvgpr_write_b32 a8, 0
	v_accvgpr_write_b32 a7, 0
	v_accvgpr_write_b32 a6, 0
	v_accvgpr_write_b32 a5, 0
	v_accvgpr_write_b32 a4, 0
	v_accvgpr_write_b32 a3, 0
	v_accvgpr_write_b32 a2, 0
	v_accvgpr_write_b32 a1, 0
	v_accvgpr_write_b32 a0, 0
	v_add_u32_e32 v3, v3, v74
	v_add_u32_e32 v16, v16, v17

.LBB8_7:
	s_load_dwordx2 s[0:1], s[0:1], 0x40
	s_waitcnt vmcnt(7)
	v_mul_u32_u24_e32 v40, 0x2400, v1
	v_accvgpr_read_b32 v39, a0
	v_accvgpr_read_b32 v38, a1
	v_lshl_or_b32 v1, v12, 2, v40
	s_waitcnt lgkmcnt(0)
	s_mul_hi_u32 s4, s0, s16
	s_mul_i32 s6, s0, s17
	s_add_i32 s4, s4, s6
	s_mul_i32 s6, s1, s16
	s_add_i32 s7, s4, s6
	s_movk_i32 s4, 0x240
	s_waitcnt vmcnt(2)
	v_accvgpr_read_b32 v37, a2
	v_accvgpr_read_b32 v36, a3
	s_waitcnt vmcnt(0)
	v_fma_f32 v12, s5, v39, v13
	v_mad_u32_u24 v1, v15, s4, v1
	v_fma_f32 v15, s5, v38, v13
	v_accvgpr_read_b32 v35, a4
	v_accvgpr_read_b32 v34, a5
	s_barrier
	ds_write2_b32 v1, v12, v15 offset1:36
	v_fma_f32 v12, s5, v37, v13
	v_fma_f32 v15, s5, v36, v13
	v_accvgpr_read_b32 v33, a6
	v_accvgpr_read_b32 v32, a7
	ds_write2_b32 v1, v12, v15 offset0:72 offset1:108
	v_fma_f32 v12, s5, v35, v13
	v_fma_f32 v15, s5, v34, v13
	v_add_u32_e32 v34, 0x400, v1
	v_accvgpr_read_b32 v31, a8
	v_accvgpr_read_b32 v30, a9
	ds_write2_b32 v34, v12, v15 offset0:32 offset1:68
	v_fma_f32 v12, s5, v33, v13
	v_fma_f32 v15, s5, v32, v13
	v_accvgpr_read_b32 v29, a10
	v_accvgpr_read_b32 v28, a11
	ds_write2_b32 v34, v12, v15 offset0:104 offset1:140
	v_fma_f32 v12, s5, v31, v13
	v_fma_f32 v15, s5, v30, v13
	v_add_u32_e32 v30, 0x800, v1
	v_accvgpr_read_b32 v27, a12
	v_accvgpr_read_b32 v26, a13
	ds_write2_b32 v30, v12, v15 offset0:64 offset1:100
	v_fma_f32 v12, s5, v29, v13
	v_fma_f32 v15, s5, v28, v13
	v_accvgpr_read_b32 v25, a14
	v_accvgpr_read_b32 v24, a15
	ds_write2_b32 v30, v12, v15 offset0:136 offset1:172
	v_fma_f32 v12, s5, v27, v13
	v_fma_f32 v15, s5, v26, v13
	v_add_u32_e32 v26, 0xc00, v1
	v_accvgpr_read_b32 v23, a16
	v_accvgpr_read_b32 v22, a17
	ds_write2_b32 v26, v12, v15 offset0:96 offset1:132
	v_fma_f32 v12, s5, v25, v13
	v_fma_f32 v15, s5, v24, v13
	v_accvgpr_read_b32 v21, a18
	v_accvgpr_read_b32 v20, a19
	ds_write2_b32 v26, v12, v15 offset0:168 offset1:204
	v_fma_f32 v12, s5, v23, v13
	v_fma_f32 v15, s5, v22, v13
	v_add_u32_e32 v22, 0x1000, v1
	v_accvgpr_read_b32 v19, a20
	v_accvgpr_read_b32 v18, a21
	ds_write2_b32 v22, v12, v15 offset0:128 offset1:164
	v_fma_f32 v12, s5, v21, v13
	v_fma_f32 v15, s5, v20, v13
	v_accvgpr_read_b32 v17, a22
	v_accvgpr_read_b32 v16, a23
	ds_write2_b32 v22, v12, v15 offset0:200 offset1:236
	v_fma_f32 v12, s5, v19, v13
	v_fma_f32 v15, s5, v18, v13
	v_add_u32_e32 v18, 0x1400, v1
	v_accvgpr_read_b32 v11, a24
	v_accvgpr_read_b32 v10, a25
	v_accvgpr_read_b32 v9, a26
	v_accvgpr_read_b32 v8, a27
	v_accvgpr_read_b32 v7, a28
	v_accvgpr_read_b32 v6, a29
	v_accvgpr_read_b32 v5, a30
	v_accvgpr_read_b32 v4, a31
	s_mul_i32 s6, s0, s16
	ds_write2_b32 v18, v12, v15 offset0:160 offset1:196
	v_fma_f32 v12, s5, v17, v13
	v_fma_f32 v15, s5, v16, v13
	v_add_u32_e32 v16, 0x1600, v1
	ds_write2_b32 v16, v12, v15 offset0:104 offset1:140
	v_fma_f32 v11, s5, v11, v13
	v_fma_f32 v10, s5, v10, v13
	v_add_u32_e32 v12, 0x1800, v1
	v_fma_f32 v9, s5, v9, v13
	v_fma_f32 v8, s5, v8, v13
	v_fma_f32 v7, s5, v7, v13
	v_fma_f32 v6, s5, v6, v13
	v_fma_f32 v5, s5, v5, v13
	v_fmac_f32_e32 v13, s5, v4
	s_lshl_b64 s[4:5], s[6:7], 2
	ds_write2_b32 v12, v11, v10 offset0:192 offset1:228
	v_add_u32_e32 v10, 0x1c00, v1
	s_add_u32 s2, s2, s4
	v_ashrrev_i32_e32 v3, 31, v2
	ds_write2_b32 v10, v9, v8 offset0:8 offset1:44
	v_add_u32_e32 v8, 0x1e00, v1
	v_add_u32_e32 v1, 0x2000, v1
	s_addc_u32 s3, s3, s5
	v_lshlrev_b32_e32 v0, 4, v0
	ds_write2_b32 v1, v5, v13 offset0:40 offset1:76
	v_lshl_add_u64 v[2:3], v[2:3], 2, s[2:3]
	v_and_b32_e32 v0, 0x70, v0
	v_mov_b32_e32 v1, 0
	ds_write2_b32 v8, v7, v6 offset0:96 offset1:132
	v_lshrrev_b32_e32 v12, 3, v14
	v_lshl_add_u64 v[8:9], v[2:3], 0, v[0:1]
	v_or_b32_e32 v0, v40, v0
	s_movk_i32 s2, 0x90
	v_mad_u32_u24 v13, v12, s2, v0
	ds_read_b128 v[0:3], v13
	v_mad_u64_u32 v[4:5], s[2:3], s0, v12, 0
	v_mov_b32_e32 v6, v5
	v_mad_u64_u32 v[6:7], s[2:3], s1, v12, v[6:7]
	v_mov_b32_e32 v5, v6
	v_lshl_add_u64 v[10:11], v[4:5], 2, v[8:9]
	ds_read_b128 v[4:7], v13 offset:1152
	s_waitcnt lgkmcnt(1)
	global_store_dwordx4 v[10:11], v[0:3], off sc1
	s_nop 1
	v_or_b32_e32 v3, 8, v12
	v_mad_u64_u32 v[0:1], s[2:3], s0, v3, 0
	v_mov_b32_e32 v2, v1
	v_mad_u64_u32 v[2:3], s[2:3], s1, v3, v[2:3]
	v_mov_b32_e32 v1, v2
	v_lshl_add_u64 v[0:1], v[0:1], 2, v[8:9]
	s_waitcnt lgkmcnt(0)
	global_store_dwordx4 v[0:1], v[4:7], off sc1
	ds_read_b128 v[0:3], v13 offset:2304
	s_nop 0
	v_or_b32_e32 v7, 16, v12
	v_mad_u64_u32 v[4:5], s[2:3], s0, v7, 0
	v_mov_b32_e32 v6, v5
	v_mad_u64_u32 v[6:7], s[2:3], s1, v7, v[6:7]
	v_mov_b32_e32 v5, v6
	v_lshl_add_u64 v[10:11], v[4:5], 2, v[8:9]
	ds_read_b128 v[4:7], v13 offset:3456
	s_waitcnt lgkmcnt(1)
	global_store_dwordx4 v[10:11], v[0:3], off sc1
	s_nop 1
	v_or_b32_e32 v3, 24, v12
	v_mad_u64_u32 v[0:1], s[2:3], s0, v3, 0
	v_mov_b32_e32 v2, v1
	v_mad_u64_u32 v[2:3], s[2:3], s1, v3, v[2:3]
	v_mov_b32_e32 v1, v2
	v_lshl_add_u64 v[0:1], v[0:1], 2, v[8:9]
	s_waitcnt lgkmcnt(0)
	global_store_dwordx4 v[0:1], v[4:7], off sc1
	ds_read_b128 v[0:3], v13 offset:4608
	s_nop 0
	v_or_b32_e32 v7, 32, v12
	v_mad_u64_u32 v[4:5], s[2:3], s0, v7, 0
	v_mov_b32_e32 v6, v5
	v_mad_u64_u32 v[6:7], s[2:3], s1, v7, v[6:7]
	v_mov_b32_e32 v5, v6
	v_lshl_add_u64 v[10:11], v[4:5], 2, v[8:9]
	ds_read_b128 v[4:7], v13 offset:5760
	s_waitcnt lgkmcnt(1)
	global_store_dwordx4 v[10:11], v[0:3], off sc1
	s_nop 1
	v_or_b32_e32 v3, 40, v12
	v_mad_u64_u32 v[0:1], s[2:3], s0, v3, 0
	v_mov_b32_e32 v2, v1
	v_mad_u64_u32 v[2:3], s[2:3], s1, v3, v[2:3]
	v_mov_b32_e32 v1, v2
	v_lshl_add_u64 v[0:1], v[0:1], 2, v[8:9]
	s_waitcnt lgkmcnt(0)
	global_store_dwordx4 v[0:1], v[4:7], off sc1
	ds_read_b128 v[0:3], v13 offset:6912
	s_nop 0
	v_or_b32_e32 v7, 48, v12
	v_mad_u64_u32 v[4:5], s[2:3], s0, v7, 0
	v_mov_b32_e32 v6, v5
	v_mad_u64_u32 v[6:7], s[2:3], s1, v7, v[6:7]
	v_mov_b32_e32 v5, v6
	v_lshl_add_u64 v[10:11], v[4:5], 2, v[8:9]
	ds_read_b128 v[4:7], v13 offset:8064
	s_waitcnt lgkmcnt(1)
	global_store_dwordx4 v[10:11], v[0:3], off sc1
	s_nop 1
	v_or_b32_e32 v3, 56, v12
	v_mad_u64_u32 v[0:1], s[2:3], s0, v3, 0
	v_mov_b32_e32 v2, v1
	v_mad_u64_u32 v[2:3], s[0:1], s1, v3, v[2:3]
	v_mov_b32_e32 v1, v2
	v_lshl_add_u64 v[0:1], v[0:1], 2, v[8:9]
	s_waitcnt lgkmcnt(0)
	global_store_dwordx4 v[0:1], v[4:7], off sc1
	s_endpgm
	s_endpgm
	s_endpgm
	s_endpgm
	s_endpgm
	s_endpgm
	s_endpgm
	s_endpgm
	s_endpgm
	s_endpgm
	s_endpgm
	s_endpgm
	s_endpgm
	s_endpgm
	s_endpgm
	s_endpgm
	s_endpgm
	s_endpgm
	s_endpgm
	s_endpgm
	s_endpgm
	s_endpgm
	s_endpgm
	s_endpgm
	s_endpgm
	s_endpgm
	s_endpgm
	s_endpgm
	s_endpgm
	s_endpgm
	s_endpgm
	s_endpgm

.LBB9_4:
	s_load_dwordx4 s[32:35], s[0:1], 0x18
	s_load_dword s36, s[0:1], 0x28
	s_load_dwordx4 s[4:7], s[0:1], 0x60
	s_load_dwordx2 s[12:13], s[0:1], 0x10
	s_ashr_i32 s2, s2, 3
	s_add_i32 s2, s3, s2
	s_abs_i32 s3, s2
	s_waitcnt lgkmcnt(0)
	s_lshl_b32 s26, s7, 7
	s_lshl_b32 s24, s26, 5
	s_mov_b32 s27, 0
	s_cmp_eq_u32 s12, 0x800
	s_cselect_b32 s25, s24, 32
	s_cselect_b32 s26, s26, 1
	s_cselect_b32 s12, 32, s12
	s_abs_i32 s14, s6
	v_cvt_f32_u32_e32 v1, s14
	s_sub_i32 s16, 0, s14
	s_xor_b32 s15, s2, s6
	s_ashr_i32 s15, s15, 31
	v_rcp_iflag_f32_e32 v1, v1
	v_lshlrev_b32_e32 v3, 3, v0
	v_lshrrev_b32_e32 v2, 2, v0
	v_and_b32_e32 v8, 24, v3
	v_mul_f32_e32 v1, 0x4f7ffffe, v1
	v_cvt_u32_f32_e32 v1, v1
	v_mov_b32_e32 v9, 0
	v_lshlrev_b32_e32 v3, 1, v8
	v_lshrrev_b32_e32 v23, 6, v0
	v_readfirstlane_b32 s17, v1
	s_mul_i32 s16, s16, s17
	s_mul_hi_u32 s16, s17, s16
	s_add_i32 s17, s17, s16
	s_mul_hi_u32 s16, s3, s17
	s_mul_i32 s17, s16, s14
	s_sub_i32 s3, s3, s17
	s_add_i32 s18, s16, 1
	s_sub_i32 s17, s3, s14
	s_cmp_ge_u32 s3, s14
	s_cselect_b32 s16, s18, s16
	s_cselect_b32 s3, s17, s3
	s_add_i32 s17, s16, 1
	s_cmp_ge_u32 s3, s14
	s_cselect_b32 s3, s17, s16
	s_abs_i32 s16, s7
	v_cvt_f32_u32_e32 v1, s16
	s_xor_b32 s3, s3, s15
	s_sub_i32 s3, s3, s15
	s_mul_i32 s6, s3, s6
	v_rcp_iflag_f32_e32 v1, v1
	s_sub_i32 s17, 0, s16
	s_sub_i32 s14, s2, s6
	s_xor_b32 s15, s3, s7
	v_mul_f32_e32 v1, 0x4f7ffffe, v1
	v_cvt_u32_f32_e32 v1, v1
	s_ashr_i32 s2, s15, 31
	s_abs_i32 s18, s3
	v_and_b32_e32 v22, 31, v0
	v_readfirstlane_b32 s6, v1
	s_mul_i32 s17, s17, s6
	s_mul_hi_u32 s15, s6, s17
	s_add_i32 s6, s6, s15
	s_mul_hi_u32 s6, s18, s6
	s_mul_i32 s15, s6, s16
	s_sub_i32 s15, s18, s15
	s_add_i32 s17, s6, 1
	s_sub_i32 s18, s15, s16
	s_cmp_ge_u32 s15, s16
	s_cselect_b32 s6, s17, s6
	s_cselect_b32 s15, s18, s15
	s_add_i32 s17, s6, 1
	s_cmp_ge_u32 s15, s16
	s_cselect_b32 s6, s17, s6
	s_xor_b32 s6, s6, s2
	s_sub_i32 s16, s6, s2
	s_mul_i32 s2, s16, s7
	s_sub_i32 s2, s3, s2
	s_lshl_b32 s15, s2, 7
	s_mul_i32 s2, s16, s4
	s_mul_i32 s26, s2, s26
	s_ashr_i32 s3, s2, 31
	v_or_b32_e32 v1, s15, v2
	s_ashr_i32 s17, s15, 31
	v_lshl_add_u64 v[4:5], s[26:27], 0, v[8:9]
	s_mul_i32 s20, s12, s17
	v_mad_u64_u32 v[4:5], s[18:19], s12, v1, v[4:5]
	v_mul_lo_u32 v1, s13, v1
	s_lshl_b64 s[6:7], s[12:13], 6
	v_add3_u32 v5, v1, v5, s20
	v_lshl_add_u64 v[6:7], v[4:5], 0, s[6:7]
	v_lshlrev_b64 v[4:5], 1, v[4:5]
	v_lshl_add_u64 v[12:13], s[10:11], 0, v[4:5]
	v_lshl_add_u64 v[14:15], s[8:9], 0, v[4:5]
	s_lshl_b64 s[6:7], s[12:13], 7
	v_lshl_add_u64 v[10:11], v[6:7], 1, s[8:9]
	v_lshl_add_u64 v[16:17], v[12:13], 0, s[6:7]
	global_load_dwordx4 v[124:127], v[14:15], off
	global_load_dwordx4 v[128:131], v[12:13], off
	global_load_dwordx4 v[132:135], v[10:11], off
	global_load_dwordx4 v[136:139], v[16:17], off
	s_load_dwordx2 s[6:7], s[0:1], 0x38
	s_movk_i32 s9, 0x50
	v_and_b32_e32 v1, 63, v0
	v_accvgpr_write_b32 a48, 0
	v_accvgpr_write_b32 a49, 0
	v_accvgpr_write_b32 a50, 0
	v_accvgpr_write_b32 a51, 0
	v_accvgpr_write_b32 a52, 0
	v_accvgpr_write_b32 a53, 0
	v_accvgpr_write_b32 a54, 0
	v_accvgpr_write_b32 a55, 0
	v_accvgpr_write_b32 a56, 0
	v_accvgpr_write_b32 a57, 0
	v_accvgpr_write_b32 a58, 0
	v_accvgpr_write_b32 a59, 0
	v_accvgpr_write_b32 a60, 0
	v_accvgpr_write_b32 a61, 0
	v_accvgpr_write_b32 a62, 0
	v_accvgpr_write_b32 a63, 0
	v_accvgpr_write_b32 a32, 0
	v_accvgpr_write_b32 a33, 0
	v_accvgpr_write_b32 a34, 0
	v_accvgpr_write_b32 a35, 0
	v_accvgpr_write_b32 a36, 0
	v_accvgpr_write_b32 a37, 0
	v_accvgpr_write_b32 a38, 0
	v_accvgpr_write_b32 a39, 0
	v_accvgpr_write_b32 a40, 0
	v_accvgpr_write_b32 a41, 0
	v_accvgpr_write_b32 a42, 0
	v_accvgpr_write_b32 a43, 0
	v_accvgpr_write_b32 a44, 0
	v_accvgpr_write_b32 a45, 0
	v_accvgpr_write_b32 a46, 0
	v_accvgpr_write_b32 a47, 0
	v_accvgpr_write_b32 a16, 0
	v_accvgpr_write_b32 a17, 0
	v_accvgpr_write_b32 a18, 0
	v_accvgpr_write_b32 a19, 0
	v_accvgpr_write_b32 a20, 0
	v_accvgpr_write_b32 a21, 0
	v_accvgpr_write_b32 a22, 0
	v_accvgpr_write_b32 a23, 0
	v_accvgpr_write_b32 a24, 0
	v_accvgpr_write_b32 a25, 0
	v_accvgpr_write_b32 a26, 0
	v_accvgpr_write_b32 a27, 0
	v_accvgpr_write_b32 a28, 0
	v_accvgpr_write_b32 a29, 0
	v_accvgpr_write_b32 a30, 0
	v_accvgpr_write_b32 a31, 0
	v_accvgpr_write_b32 a0, 0
	v_accvgpr_write_b32 a1, 0
	v_accvgpr_write_b32 a2, 0
	v_accvgpr_write_b32 a3, 0
	v_accvgpr_write_b32 a4, 0
	v_accvgpr_write_b32 a5, 0
	v_accvgpr_write_b32 a6, 0
	v_accvgpr_write_b32 a7, 0
	v_accvgpr_write_b32 a8, 0
	v_accvgpr_write_b32 a9, 0
	v_accvgpr_write_b32 a10, 0
	v_accvgpr_write_b32 a11, 0
	v_accvgpr_write_b32 a12, 0
	v_accvgpr_write_b32 a13, 0
	v_accvgpr_write_b32 a14, 0
	v_accvgpr_write_b32 a15, 0
	v_bfe_u32 v24, v0, 5, 1
	v_mad_u32_u24 v112, v2, s9, v3
	s_mov_b32 s10, s36
	s_lshr_b32 s3, s3, 28
	s_ashr_i32 s8, s4, 31
	s_add_i32 s2, s2, s3
	s_lshr_b32 s8, s8, 27
	s_waitcnt lgkmcnt(0)
	s_ashr_i32 s12, s10, 31
	s_lshr_b32 s12, s12, 28
	s_ashr_i32 s2, s2, 4
	s_add_i32 s4, s4, s8
	s_add_i32 s10, s10, s12
	s_ashr_i32 s3, s2, 31
	s_ashr_i32 s4, s4, 5
	v_lshl_or_b32 v6, s14, 2, v23
	s_ashr_i32 s10, s10, 4
	v_mov_b32_e32 v4, s2
	v_mov_b32_e32 v5, s3
	s_add_i32 s8, s4, -1
	v_mad_i64_i32 v[4:5], s[2:3], v6, s10, v[4:5]
	s_min_i32 s11, s8, 2
	v_lshlrev_b64 v[4:5], 10, v[4:5]
	v_lshl_or_b32 v4, v1, 4, v4
	s_mul_i32 s2, s11, s25
	v_lshl_add_u64 v[18:19], s[32:33], 0, v[4:5]
	s_ashr_i32 s3, s2, 31
	s_lshl_b32 s28, s25, 1
	s_mov_b32 s29, 0
	v_lshl_add_u64 v[116:117], v[14:15], 0, s[28:29]
	v_lshl_add_u64 v[118:119], v[12:13], 0, s[28:29]
	v_lshl_add_u64 v[120:121], v[10:11], 0, s[28:29]
	v_lshl_add_u64 v[122:123], v[16:17], 0, s[28:29]
	global_load_dwordx4 v[44:47], v[116:117], off
	global_load_dwordx4 v[48:51], v[118:119], off
	global_load_dwordx4 v[32:35], v[120:121], off
	global_load_dwordx4 v[28:31], v[122:123], off
	v_lshl_add_u64 v[20:21], s[34:35], 0, v[4:5]
	global_load_dwordx4 v[64:67], v[18:19], off
	global_load_dwordx4 v[36:39], v[18:19], off offset:1024
	global_load_dwordx4 v[80:83], v[20:21], off
	global_load_dwordx4 v[40:43], v[20:21], off offset:1024
	global_load_dwordx4 v[68:71], v[18:19], off offset:2048
	global_load_dwordx4 v[76:79], v[20:21], off offset:2048
	s_lshl_b64 s[2:3], s[2:3], 1
	v_lshl_add_u64 v[26:27], v[14:15], 0, s[2:3]
	v_lshl_add_u64 v[4:5], v[10:11], 0, s[2:3]
	v_lshl_add_u64 v[6:7], v[12:13], 0, s[2:3]
	v_lshl_add_u64 v[8:9], v[16:17], 0, s[2:3]
	global_load_dwordx4 v[60:63], v[26:27], off
	global_load_dwordx4 v[56:59], v[4:5], off
	global_load_dwordx4 v[72:75], v[6:7], off
	global_load_dwordx4 v[52:55], v[8:9], off
	s_waitcnt vmcnt(17)
	ds_write_b128 v112, v[124:127]
	s_waitcnt vmcnt(16)
	ds_write_b128 v112, v[128:131] offset:10240
	s_waitcnt vmcnt(15)
	ds_write_b128 v112, v[132:135] offset:5120
	s_waitcnt vmcnt(14)
	ds_write_b128 v112, v[136:139] offset:15360
	s_waitcnt lgkmcnt(0)
	s_barrier
	v_lshlrev_b32_e32 v4, 4, v24
	v_mad_u32_u24 v6, v22, s9, v4
	ds_read_b128 v[84:87], v6 offset:7680
	ds_read_b128 v[92:95], v6 offset:5120
	ds_read_b128 v[88:91], v6 offset:17920
	ds_read_b128 v[96:99], v6 offset:15360
	ds_read_b128 v[100:103], v6 offset:2560
	ds_read_b128 v[104:107], v6
	ds_read_b128 v[108:111], v6 offset:12800
	ds_read_b128 v[112:115], v6 offset:10240
	v_mul_u32_u24_e32 v2, 0x50, v2
	v_mul_u32_u24_e32 v5, 0x50, v22
	s_mov_b32 s2, 4
	v_accvgpr_write_b32 a15, 0
	v_accvgpr_write_b32 a14, 0
	v_accvgpr_write_b32 a13, 0
	v_accvgpr_write_b32 a12, 0
	v_accvgpr_write_b32 a11, 0
	v_accvgpr_write_b32 a10, 0
	v_accvgpr_write_b32 a9, 0
	v_accvgpr_write_b32 a8, 0
	v_accvgpr_write_b32 a7, 0
	v_accvgpr_write_b32 a6, 0
	v_accvgpr_write_b32 a5, 0
	v_accvgpr_write_b32 a4, 0
	v_accvgpr_write_b32 a3, 0
	v_accvgpr_write_b32 a2, 0
	v_accvgpr_write_b32 a1, 0
	v_accvgpr_write_b32 a0, 0
	v_accvgpr_write_b32 a31, 0
	v_accvgpr_write_b32 a30, 0
	v_accvgpr_write_b32 a29, 0
	v_accvgpr_write_b32 a28, 0
	v_accvgpr_write_b32 a27, 0
	v_accvgpr_write_b32 a26, 0
	v_accvgpr_write_b32 a25, 0
	v_accvgpr_write_b32 a24, 0
	v_accvgpr_write_b32 a23, 0
	v_accvgpr_write_b32 a22, 0
	v_accvgpr_write_b32 a21, 0
	v_accvgpr_write_b32 a20, 0
	v_accvgpr_write_b32 a19, 0
	v_accvgpr_write_b32 a18, 0
	v_accvgpr_write_b32 a17, 0
	v_accvgpr_write_b32 a16, 0
	v_accvgpr_write_b32 a47, 0
	v_accvgpr_write_b32 a46, 0
	v_accvgpr_write_b32 a45, 0
	v_accvgpr_write_b32 a44, 0
	v_accvgpr_write_b32 a43, 0
	v_accvgpr_write_b32 a42, 0
	v_accvgpr_write_b32 a41, 0
	v_accvgpr_write_b32 a40, 0
	v_accvgpr_write_b32 a39, 0
	v_accvgpr_write_b32 a38, 0
	v_accvgpr_write_b32 a37, 0
	v_accvgpr_write_b32 a36, 0
	v_accvgpr_write_b32 a35, 0
	v_accvgpr_write_b32 a34, 0
	v_accvgpr_write_b32 a33, 0
	v_accvgpr_write_b32 a32, 0
	v_accvgpr_write_b32 a63, 0
	v_accvgpr_write_b32 a62, 0
	v_accvgpr_write_b32 a61, 0
	v_accvgpr_write_b32 a60, 0
	v_accvgpr_write_b32 a59, 0
	v_accvgpr_write_b32 a58, 0
	v_accvgpr_write_b32 a57, 0
	v_accvgpr_write_b32 a56, 0
	v_accvgpr_write_b32 a55, 0
	v_accvgpr_write_b32 a54, 0
	v_accvgpr_write_b32 a53, 0
	v_accvgpr_write_b32 a52, 0
	v_accvgpr_write_b32 a51, 0
	v_accvgpr_write_b32 a50, 0
	v_accvgpr_write_b32 a49, 0
	v_accvgpr_write_b32 a48, 0
	v_add_u32_e32 v25, v4, v5
	v_add_u32_e32 v26, v3, v2
.LBB9_6:
	s_waitcnt vmcnt(9) lgkmcnt(0)
	v_mfma_f32_32x32x16_f16 a[0:15], v[112:115], v[64:67], a[0:15]
	s_add_i32 s3, s2, -3
	s_min_i32 s3, s3, s8
	s_lshl_b32 s3, s3, 1
	ds_read_b128 v[116:119], v25 offset:10272
	s_or_b32 s10, s3, 1
	s_ashr_i32 s11, s10, 31
	s_lshl_b64 s[10:11], s[10:11], 10
	v_lshl_add_u64 v[2:3], v[18:19], 0, s[10:11]
	v_lshl_add_u64 v[6:7], v[20:21], 0, s[10:11]
	s_waitcnt vmcnt(7)
	v_mfma_f32_32x32x16_f16 a[0:15], v[104:107], v[80:83], a[0:15]
	ds_read_b128 v[112:115], v25 offset:32
	v_mfma_f32_32x32x16_f16 a[0:15], v[104:107], v[64:67], a[0:15]
	ds_read_b128 v[120:123], v25 offset:12832
	ds_write_b128 v26, v[44:47] offset:20480
	v_mfma_f32_32x32x16_f16 a[16:31], v[108:111], v[64:67], a[16:31]
	ds_read_b128 v[104:107], v25 offset:2592
	v_mfma_f32_32x32x16_f16 a[16:31], v[100:103], v[80:83], a[16:31]
	ds_read_b128 v[108:111], v25 offset:15392
	ds_write_b128 v26, v[48:51] offset:30720
	v_mfma_f32_32x32x16_f16 a[16:31], v[100:103], v[64:67], a[16:31]
	ds_read_b128 v[124:127], v25 offset:5152
	v_mfma_f32_32x32x16_f16 a[32:47], v[96:99], v[64:67], a[32:47]
	ds_read_b128 v[100:103], v25 offset:17952
	ds_write_b128 v26, v[32:35] offset:25600
	v_mfma_f32_32x32x16_f16 a[32:47], v[92:95], v[80:83], a[32:47]
	ds_read_b128 v[96:99], v25 offset:7712
	v_mfma_f32_32x32x16_f16 a[32:47], v[92:95], v[64:67], a[32:47]
	ds_write_b128 v26, v[28:31] offset:35840
	global_load_dwordx4 v[2:5], v[2:3], off
	s_nop 0
	global_load_dwordx4 v[6:9], v[6:7], off
	v_mfma_f32_32x32x16_f16 a[48:63], v[88:91], v[64:67], a[48:63]
	v_mfma_f32_32x32x16_f16 a[48:63], v[84:87], v[80:83], a[48:63]
	v_mfma_f32_32x32x16_f16 a[48:63], v[84:87], v[64:67], a[48:63]
	s_add_i32 s3, s2, -1
	s_min_i32 s9, s3, s8
	s_mul_i32 s10, s9, s25
	s_ashr_i32 s11, s10, 31
	s_lshl_b64 s[10:11], s[10:11], 1
	v_lshl_add_u64 v[28:29], v[14:15], 0, s[10:11]
	s_waitcnt lgkmcnt(0)
	s_barrier
	global_load_dwordx4 v[44:47], v[28:29], off
	v_mfma_f32_32x32x16_f16 a[0:15], v[116:119], v[36:39], a[0:15]
	s_add_i32 s3, s2, -2
	v_lshl_add_u64 v[28:29], v[10:11], 0, s[10:11]
	v_lshl_add_u64 v[30:31], v[12:13], 0, s[10:11]
	v_lshl_add_u64 v[64:65], v[16:17], 0, s[10:11]
	s_min_i32 s10, s3, s8
	ds_read_b128 v[84:87], v25 offset:30720
	s_lshl_b32 s10, s10, 1
	s_ashr_i32 s11, s10, 31
	s_lshl_b64 s[12:13], s[10:11], 10
	v_lshl_add_u64 v[66:67], v[18:19], 0, s[12:13]
	v_lshl_add_u64 v[80:81], v[20:21], 0, s[12:13]
	global_load_dwordx4 v[48:51], v[30:31], off
	s_waitcnt vmcnt(10)
	v_mfma_f32_32x32x16_f16 a[0:15], v[112:115], v[40:43], a[0:15]
	ds_read_b128 v[88:91], v25 offset:20480
	global_load_dwordx4 v[32:35], v[28:29], off
	v_mfma_f32_32x32x16_f16 a[0:15], v[112:115], v[36:39], a[0:15]
	ds_read_b128 v[92:95], v25 offset:33280
	global_load_dwordx4 v[28:31], v[64:65], off
	v_mfma_f32_32x32x16_f16 a[16:31], v[120:123], v[36:39], a[16:31]
	ds_read_b128 v[112:115], v25 offset:23040
	v_mfma_f32_32x32x16_f16 a[16:31], v[104:107], v[40:43], a[16:31]
	ds_read_b128 v[116:119], v25 offset:35840
	v_mfma_f32_32x32x16_f16 a[16:31], v[104:107], v[36:39], a[16:31]
	ds_read_b128 v[120:123], v25 offset:25600
	v_mfma_f32_32x32x16_f16 a[32:47], v[108:111], v[36:39], a[32:47]
	ds_read_b128 v[104:107], v25 offset:38400
	v_mfma_f32_32x32x16_f16 a[32:47], v[124:127], v[40:43], a[32:47]
	ds_read_b128 v[108:111], v25 offset:28160
	v_mfma_f32_32x32x16_f16 a[32:47], v[124:127], v[36:39], a[32:47]
	global_load_dwordx4 v[64:67], v[66:67], off
	s_nop 0
	global_load_dwordx4 v[80:83], v[80:81], off
	v_mfma_f32_32x32x16_f16 a[48:63], v[100:103], v[36:39], a[48:63]
	v_mfma_f32_32x32x16_f16 a[48:63], v[96:99], v[40:43], a[48:63]
	v_mfma_f32_32x32x16_f16 a[48:63], v[96:99], v[36:39], a[48:63]
	s_waitcnt vmcnt(9) lgkmcnt(7)
	v_mfma_f32_32x32x16_f16 a[0:15], v[84:87], v[68:71], a[0:15]
	ds_read_b128 v[96:99], v25 offset:30752
	s_or_b32 s10, s10, 1
	s_ashr_i32 s11, s10, 31
	s_lshl_b64 s[10:11], s[10:11], 10
	v_lshl_add_u64 v[36:37], v[18:19], 0, s[10:11]
	v_lshl_add_u64 v[40:41], v[20:21], 0, s[10:11]
	s_waitcnt vmcnt(8) lgkmcnt(7)
	v_mfma_f32_32x32x16_f16 a[0:15], v[88:91], v[76:79], a[0:15]
	ds_read_b128 v[84:87], v25 offset:20512
	v_mfma_f32_32x32x16_f16 a[0:15], v[88:91], v[68:71], a[0:15]
	ds_read_b128 v[124:127], v25 offset:33312
	s_waitcnt vmcnt(11)
	ds_write_b128 v26, v[60:63]
	s_waitcnt lgkmcnt(9)
	v_mfma_f32_32x32x16_f16 a[16:31], v[92:95], v[68:71], a[16:31]
	ds_read_b128 v[88:91], v25 offset:23072
	s_waitcnt lgkmcnt(9)
	v_mfma_f32_32x32x16_f16 a[16:31], v[112:115], v[76:79], a[16:31]
	ds_read_b128 v[128:131], v25 offset:35872
	s_waitcnt vmcnt(9)
	ds_write_b128 v26, v[72:75] offset:10240
	v_mfma_f32_32x32x16_f16 a[16:31], v[112:115], v[68:71], a[16:31]
	ds_read_b128 v[132:135], v25 offset:25632
	s_waitcnt lgkmcnt(11)
	v_mfma_f32_32x32x16_f16 a[32:47], v[116:119], v[68:71], a[32:47]
	ds_read_b128 v[136:139], v25 offset:38432
	ds_write_b128 v26, v[56:59] offset:5120
	s_waitcnt lgkmcnt(12)
	v_mfma_f32_32x32x16_f16 a[32:47], v[120:123], v[76:79], a[32:47]
	ds_read_b128 v[116:119], v25 offset:28192
	v_mfma_f32_32x32x16_f16 a[32:47], v[120:123], v[68:71], a[32:47]
	s_waitcnt vmcnt(10)
	ds_write_b128 v26, v[52:55] offset:15360
	global_load_dwordx4 v[36:39], v[36:37], off
	s_nop 0
	global_load_dwordx4 v[40:43], v[40:41], off
	s_waitcnt lgkmcnt(13)
	v_mfma_f32_32x32x16_f16 a[48:63], v[104:107], v[68:71], a[48:63]
	s_waitcnt lgkmcnt(12)
	v_mfma_f32_32x32x16_f16 a[48:63], v[108:111], v[76:79], a[48:63]
	v_mfma_f32_32x32x16_f16 a[48:63], v[108:111], v[68:71], a[48:63]
	s_min_i32 s10, s2, s8
	s_mul_i32 s10, s10, s25
	s_ashr_i32 s11, s10, 31
	s_lshl_b64 s[10:11], s[10:11], 1
	v_lshl_add_u64 v[52:53], v[14:15], 0, s[10:11]
	s_waitcnt lgkmcnt(0)
	s_barrier
	global_load_dwordx4 v[60:63], v[52:53], off
	s_waitcnt vmcnt(10)
	v_mfma_f32_32x32x16_f16 a[0:15], v[96:99], v[2:5], a[0:15]
	ds_read_b128 v[112:115], v25 offset:10240
	v_lshl_add_u64 v[52:53], v[10:11], 0, s[10:11]
	v_lshl_add_u64 v[54:55], v[12:13], 0, s[10:11]
	v_lshl_add_u64 v[68:69], v[16:17], 0, s[10:11]
	s_lshl_b32 s10, s9, 1
	s_ashr_i32 s11, s10, 31
	s_lshl_b64 s[10:11], s[10:11], 10
	v_lshl_add_u64 v[70:71], v[18:19], 0, s[10:11]
	v_lshl_add_u64 v[76:77], v[20:21], 0, s[10:11]
	global_load_dwordx4 v[72:75], v[54:55], off
	s_waitcnt vmcnt(10)
	v_mfma_f32_32x32x16_f16 a[0:15], v[84:87], v[6:9], a[0:15]
	ds_read_b128 v[104:107], v25
	global_load_dwordx4 v[56:59], v[52:53], off
	v_mfma_f32_32x32x16_f16 a[0:15], v[84:87], v[2:5], a[0:15]
	ds_read_b128 v[108:111], v25 offset:12800
	global_load_dwordx4 v[52:55], v[68:69], off
	v_mfma_f32_32x32x16_f16 a[16:31], v[124:127], v[2:5], a[16:31]
	ds_read_b128 v[100:103], v25 offset:2560
	v_mfma_f32_32x32x16_f16 a[16:31], v[88:91], v[6:9], a[16:31]
	ds_read_b128 v[96:99], v25 offset:15360
	v_mfma_f32_32x32x16_f16 a[16:31], v[88:91], v[2:5], a[16:31]
	ds_read_b128 v[92:95], v25 offset:5120
	v_mfma_f32_32x32x16_f16 a[32:47], v[128:131], v[2:5], a[32:47]
	ds_read_b128 v[88:91], v25 offset:17920
	v_mfma_f32_32x32x16_f16 a[32:47], v[132:135], v[6:9], a[32:47]
	ds_read_b128 v[84:87], v25 offset:7680
	v_mfma_f32_32x32x16_f16 a[32:47], v[132:135], v[2:5], a[32:47]
	global_load_dwordx4 v[68:71], v[70:71], off
	s_nop 0
	global_load_dwordx4 v[76:79], v[76:77], off
	v_mfma_f32_32x32x16_f16 a[48:63], v[136:139], v[2:5], a[48:63]
	v_mfma_f32_32x32x16_f16 a[48:63], v[116:119], v[6:9], a[48:63]
	v_mfma_f32_32x32x16_f16 a[48:63], v[116:119], v[2:5], a[48:63]
	s_add_i32 s2, s2, 2
	s_cmp_lt_i32 s3, s4
	s_cbranch_scc1 .LBB9_6
.LBB9_7:
	s_load_dwordx4 s[0:3], s[0:1], 0x40
	s_ashr_i32 s4, s16, 31
	s_waitcnt vmcnt(1)
	v_lshlrev_b32_e32 v69, 5, v23
	v_lshl_or_b32 v70, s14, 7, v69
	v_mul_u32_u24_e32 v23, 0x2400, v23
	s_waitcnt lgkmcnt(0)
	s_mul_hi_u32 s8, s2, s16
	s_mul_i32 s4, s2, s4
	s_add_i32 s4, s8, s4
	s_mul_i32 s3, s3, s16
	s_add_i32 s3, s4, s3
	s_mul_i32 s2, s2, s16
	s_lshl_b64 s[2:3], s[2:3], 2
	s_add_u32 s4, s6, s2
	s_addc_u32 s6, s7, s3
	s_mul_hi_u32 s2, s0, s15
	s_mul_i32 s3, s0, s17
	s_add_i32 s2, s2, s3
	s_mul_i32 s3, s1, s15
	s_add_i32 s3, s2, s3
	s_mul_i32 s2, s0, s15
	s_lshl_b64 s[2:3], s[2:3], 2
	s_add_u32 s2, s4, s2
	s_addc_u32 s3, s6, s3
	v_ashrrev_i32_e32 v71, 31, v70
	v_lshlrev_b32_e32 v0, 4, v0
	v_accvgpr_read_b32 v68, a0
	v_accvgpr_read_b32 v67, a1
	v_lshl_add_u64 v[70:71], v[70:71], 2, s[2:3]
	v_and_b32_e32 v72, 0x70, v0
	v_mov_b32_e32 v73, 0
	v_lshl_or_b32 v22, v22, 2, v23
	s_movk_i32 s2, 0x240
	v_accvgpr_read_b32 v66, a2
	v_lshrrev_b32_e32 v69, 3, v1
	v_lshl_add_u64 v[0:1], v[70:71], 0, v[72:73]
	v_or_b32_e32 v70, v23, v72
	v_fma_f32 v23, s5, v68, 0
	v_mad_u32_u24 v68, v24, s2, v22
	v_fma_f32 v22, s5, v67, 0
	v_accvgpr_read_b32 v65, a3
	s_barrier
	ds_write_b32 v68, v22 offset:144
	v_fma_f32 v22, s5, v66, 0
	v_accvgpr_read_b32 v64, a4
	ds_write_b32 v68, v22 offset:288
	v_fma_f32 v22, s5, v65, 0
	v_accvgpr_read_b32 v63, a5
	ds_write_b32 v68, v22 offset:432
	v_fma_f32 v22, s5, v64, 0
	v_accvgpr_read_b32 v62, a6
	ds_write_b32 v68, v22 offset:1152
	v_fma_f32 v22, s5, v63, 0
	v_accvgpr_read_b32 v61, a7
	ds_write_b32 v68, v22 offset:1296
	v_fma_f32 v22, s5, v62, 0
	v_accvgpr_read_b32 v60, a8
	ds_write_b32 v68, v22 offset:1440
	v_fma_f32 v22, s5, v61, 0
	v_accvgpr_read_b32 v59, a9
	ds_write_b32 v68, v22 offset:1584
	v_fma_f32 v22, s5, v60, 0
	v_accvgpr_read_b32 v58, a10
	ds_write_b32 v68, v22 offset:2304
	v_fma_f32 v22, s5, v59, 0
	v_accvgpr_read_b32 v57, a11
	ds_write_b32 v68, v22 offset:2448
	v_fma_f32 v22, s5, v58, 0
	v_accvgpr_read_b32 v56, a12
	ds_write_b32 v68, v22 offset:2592
	v_fma_f32 v22, s5, v57, 0
	v_accvgpr_read_b32 v55, a13
	ds_write_b32 v68, v22 offset:2736
	v_fma_f32 v22, s5, v56, 0
	v_accvgpr_read_b32 v54, a14
	ds_write_b32 v68, v22 offset:3456
	v_fma_f32 v22, s5, v55, 0
	v_accvgpr_read_b32 v53, a15
	ds_write_b32 v68, v22 offset:3600
	v_fma_f32 v22, s5, v54, 0
	v_accvgpr_read_b32 v52, a16
	ds_write_b32 v68, v22 offset:3744
	v_fma_f32 v22, s5, v53, 0
	v_accvgpr_read_b32 v51, a17
	ds_write_b32 v68, v22 offset:3888
	v_fma_f32 v22, s5, v52, 0
	v_accvgpr_read_b32 v50, a18
	ds_write_b32 v68, v22 offset:4608
	v_fma_f32 v22, s5, v51, 0
	v_accvgpr_read_b32 v49, a19
	ds_write_b32 v68, v22 offset:4752
	v_fma_f32 v22, s5, v50, 0
	v_accvgpr_read_b32 v48, a20
	ds_write_b32 v68, v22 offset:4896
	v_fma_f32 v22, s5, v49, 0
	v_accvgpr_read_b32 v47, a21
	ds_write_b32 v68, v22 offset:5040
	v_fma_f32 v22, s5, v48, 0
	v_accvgpr_read_b32 v46, a22
	ds_write_b32 v68, v22 offset:5760
	v_fma_f32 v22, s5, v47, 0
	v_accvgpr_read_b32 v45, a23
	ds_write_b32 v68, v22 offset:5904
	v_fma_f32 v22, s5, v46, 0
	v_accvgpr_read_b32 v44, a24
	ds_write_b32 v68, v22 offset:6048
	v_fma_f32 v22, s5, v45, 0
	v_accvgpr_read_b32 v43, a25
	ds_write_b32 v68, v22 offset:6192
	v_fma_f32 v22, s5, v44, 0
	v_accvgpr_read_b32 v42, a26
	ds_write_b32 v68, v22 offset:6912
	v_fma_f32 v22, s5, v43, 0
	v_accvgpr_read_b32 v41, a27
	ds_write_b32 v68, v22 offset:7056
	v_fma_f32 v22, s5, v42, 0
	v_accvgpr_read_b32 v40, a28
	ds_write_b32 v68, v22 offset:7200
	v_fma_f32 v22, s5, v41, 0
	v_accvgpr_read_b32 v39, a29
	ds_write_b32 v68, v22 offset:7344
	v_fma_f32 v22, s5, v40, 0
	v_accvgpr_read_b32 v38, a30
	ds_write_b32 v68, v22 offset:8064
	v_fma_f32 v22, s5, v39, 0
	v_accvgpr_read_b32 v37, a31
	ds_write_b32 v68, v22 offset:8208
	v_fma_f32 v22, s5, v38, 0
	s_movk_i32 s4, 0x90
	ds_write_b32 v68, v22 offset:8352
	v_fma_f32 v22, s5, v37, 0
	v_mad_u32_u24 v71, v69, s4, v70
	ds_write_b32 v68, v23
	ds_write_b32 v68, v22 offset:8496
	ds_read_b128 v[38:41], v71
	v_mad_u64_u32 v[22:23], s[2:3], s0, v69, 0
	v_accvgpr_read_b32 v25, a43
	v_mov_b32_e32 v24, v23
	v_mad_u64_u32 v[42:43], s[2:3], s1, v69, v[24:25]
	v_mov_b32_e32 v23, v42
	v_or_b32_e32 v37, 8, v69
	v_lshl_add_u64 v[22:23], v[22:23], 2, v[0:1]
	v_mad_u32_u24 v46, v37, s4, v70
	ds_read_b128 v[42:45], v46
	s_waitcnt lgkmcnt(1)
	global_store_dwordx4 v[22:23], v[38:41], off sc1
	v_mad_u64_u32 v[22:23], s[2:3], s0, v37, 0
	v_mov_b32_e32 v24, v23
	v_mad_u64_u32 v[38:39], s[2:3], s1, v37, v[24:25]
	v_mov_b32_e32 v23, v38
	v_lshl_add_u64 v[22:23], v[22:23], 2, v[0:1]
	v_or_b32_e32 v37, 16, v69
	ds_read_b128 v[38:41], v46 offset:1152
	s_waitcnt lgkmcnt(1)
	global_store_dwordx4 v[22:23], v[42:45], off sc1
	v_mad_u64_u32 v[22:23], s[2:3], s0, v37, 0
	v_mov_b32_e32 v24, v23
	v_mad_u64_u32 v[42:43], s[2:3], s1, v37, v[24:25]
	v_mov_b32_e32 v23, v42
	v_lshl_add_u64 v[22:23], v[22:23], 2, v[0:1]
	v_or_b32_e32 v37, 24, v69
	ds_read_b128 v[42:45], v46 offset:2304
	s_waitcnt lgkmcnt(1)
	global_store_dwordx4 v[22:23], v[38:41], off sc1
	v_mad_u64_u32 v[22:23], s[2:3], s0, v37, 0
	v_mov_b32_e32 v24, v23
	v_mad_u64_u32 v[38:39], s[2:3], s1, v37, v[24:25]
	v_mov_b32_e32 v23, v38
	v_lshl_add_u64 v[22:23], v[22:23], 2, v[0:1]
	v_or_b32_e32 v37, 32, v69
	ds_read_b128 v[38:41], v46 offset:3456
	s_waitcnt lgkmcnt(1)
	global_store_dwordx4 v[22:23], v[42:45], off sc1
	v_mad_u64_u32 v[22:23], s[2:3], s0, v37, 0
	v_mov_b32_e32 v24, v23
	v_mad_u64_u32 v[42:43], s[2:3], s1, v37, v[24:25]
	v_mov_b32_e32 v23, v42
	v_lshl_add_u64 v[22:23], v[22:23], 2, v[0:1]
	v_or_b32_e32 v37, 40, v69
	ds_read_b128 v[42:45], v46 offset:4608
	s_waitcnt lgkmcnt(1)
	global_store_dwordx4 v[22:23], v[38:41], off sc1
	v_mad_u64_u32 v[22:23], s[2:3], s0, v37, 0
	v_mov_b32_e32 v24, v23
	v_mad_u64_u32 v[38:39], s[2:3], s1, v37, v[24:25]
	v_mov_b32_e32 v23, v38
	v_lshl_add_u64 v[22:23], v[22:23], 2, v[0:1]
	v_or_b32_e32 v37, 48, v69
	ds_read_b128 v[38:41], v46 offset:5760
	s_waitcnt lgkmcnt(1)
	global_store_dwordx4 v[22:23], v[42:45], off sc1
	v_mad_u64_u32 v[22:23], s[2:3], s0, v37, 0
	v_mov_b32_e32 v24, v23
	v_mad_u64_u32 v[42:43], s[2:3], s1, v37, v[24:25]
	v_mov_b32_e32 v23, v42
	v_lshl_add_u64 v[22:23], v[22:23], 2, v[0:1]
	v_or_b32_e32 v37, 56, v69
	ds_read_b128 v[42:45], v46 offset:6912
	s_waitcnt lgkmcnt(1)
	global_store_dwordx4 v[22:23], v[38:41], off sc1
	v_mad_u64_u32 v[22:23], s[2:3], s0, v37, 0
	v_mov_b32_e32 v24, v23
	v_mad_u64_u32 v[38:39], s[2:3], s1, v37, v[24:25]
	v_mov_b32_e32 v23, v38
	v_accvgpr_read_b32 v36, a32
	v_lshl_add_u64 v[22:23], v[22:23], 2, v[0:1]
	v_accvgpr_read_b32 v35, a33
	s_waitcnt lgkmcnt(0)
	global_store_dwordx4 v[22:23], v[42:45], off sc1
	v_fma_f32 v22, s5, v36, 0
	v_accvgpr_read_b32 v34, a34
	ds_write_b32 v68, v22
	v_fma_f32 v22, s5, v35, 0
	v_accvgpr_read_b32 v33, a35
	ds_write_b32 v68, v22 offset:144
	v_fma_f32 v22, s5, v34, 0
	v_accvgpr_read_b32 v32, a36
	ds_write_b32 v68, v22 offset:288
	v_fma_f32 v22, s5, v33, 0
	v_accvgpr_read_b32 v31, a37
	ds_write_b32 v68, v22 offset:432
	v_fma_f32 v22, s5, v32, 0
	v_accvgpr_read_b32 v30, a38
	ds_write_b32 v68, v22 offset:1152
	v_fma_f32 v22, s5, v31, 0
	v_accvgpr_read_b32 v29, a39
	ds_write_b32 v68, v22 offset:1296
	v_fma_f32 v22, s5, v30, 0
	v_accvgpr_read_b32 v28, a40
	ds_write_b32 v68, v22 offset:1440
	v_fma_f32 v22, s5, v29, 0
	v_accvgpr_read_b32 v27, a41
	ds_write_b32 v68, v22 offset:1584
	v_fma_f32 v22, s5, v28, 0
	v_accvgpr_read_b32 v26, a42
	ds_write_b32 v68, v22 offset:2304
	v_fma_f32 v22, s5, v27, 0
	v_accvgpr_read_b32 v17, a48
	v_accvgpr_read_b32 v16, a49
	v_accvgpr_read_b32 v15, a50
	v_accvgpr_read_b32 v14, a51
	v_accvgpr_read_b32 v13, a52
	v_accvgpr_read_b32 v12, a53
	v_accvgpr_read_b32 v11, a54
	v_accvgpr_read_b32 v10, a55
	v_accvgpr_read_b32 v9, a56
	v_accvgpr_read_b32 v8, a57
	v_accvgpr_read_b32 v7, a58
	v_accvgpr_read_b32 v6, a59
	v_accvgpr_read_b32 v5, a60
	v_accvgpr_read_b32 v4, a61
	v_accvgpr_read_b32 v3, a62
	v_accvgpr_read_b32 v2, a63
	v_accvgpr_read_b32 v21, a44
	v_accvgpr_read_b32 v20, a45
	v_accvgpr_read_b32 v19, a46
	v_accvgpr_read_b32 v18, a47
	ds_write_b32 v68, v22 offset:2448
	v_fma_f32 v22, s5, v26, 0
	ds_write_b32 v68, v22 offset:2592
	v_fma_f32 v22, s5, v25, 0
	v_fma_f32 v21, s5, v21, 0
	v_fma_f32 v20, s5, v20, 0
	v_fma_f32 v19, s5, v19, 0
	v_fma_f32 v18, s5, v18, 0
	v_fma_f32 v17, s5, v17, 0
	v_fma_f32 v16, s5, v16, 0
	v_fma_f32 v15, s5, v15, 0
	v_fma_f32 v14, s5, v14, 0
	v_fma_f32 v13, s5, v13, 0
	v_fma_f32 v12, s5, v12, 0
	v_fma_f32 v11, s5, v11, 0
	v_fma_f32 v10, s5, v10, 0
	v_fma_f32 v9, s5, v9, 0
	v_fma_f32 v8, s5, v8, 0
	v_fma_f32 v7, s5, v7, 0
	v_fma_f32 v6, s5, v6, 0
	v_fma_f32 v5, s5, v5, 0
	v_fma_f32 v4, s5, v4, 0
	v_fma_f32 v3, s5, v3, 0
	v_fma_f32 v2, s5, v2, 0
	ds_write_b32 v68, v22 offset:2736
	ds_write_b32 v68, v21 offset:3456
	ds_write_b32 v68, v20 offset:3600
	ds_write_b32 v68, v19 offset:3744
	ds_write_b32 v68, v18 offset:3888
	ds_write_b32 v68, v17 offset:4608
	ds_write_b32 v68, v16 offset:4752
	ds_write_b32 v68, v15 offset:4896
	ds_write_b32 v68, v14 offset:5040
	ds_write_b32 v68, v13 offset:5760
	ds_write_b32 v68, v12 offset:5904
	ds_write_b32 v68, v11 offset:6048
	ds_write_b32 v68, v10 offset:6192
	ds_write_b32 v68, v9 offset:6912
	ds_write_b32 v68, v8 offset:7056
	ds_write_b32 v68, v7 offset:7200
	ds_write_b32 v68, v6 offset:7344
	ds_write_b32 v68, v5 offset:8064
	ds_write_b32 v68, v4 offset:8208
	ds_write_b32 v68, v3 offset:8352
	ds_write_b32 v68, v2 offset:8496
	v_or_b32_e32 v9, 64, v69
	ds_read_b128 v[2:5], v71
	v_mad_u64_u32 v[6:7], s[2:3], s0, v9, 0
	v_mov_b32_e32 v8, v7
	v_mad_u64_u32 v[8:9], s[2:3], s1, v9, v[8:9]
	v_mov_b32_e32 v7, v8
	v_lshl_add_u64 v[10:11], v[6:7], 2, v[0:1]
	ds_read_b128 v[6:9], v46
	s_waitcnt lgkmcnt(1)
	global_store_dwordx4 v[10:11], v[2:5], off sc1
	s_nop 1
	v_or_b32_e32 v5, 0x48, v69
	v_mad_u64_u32 v[2:3], s[2:3], s0, v5, 0
	v_mov_b32_e32 v4, v3
	v_mad_u64_u32 v[4:5], s[2:3], s1, v5, v[4:5]
	v_mov_b32_e32 v3, v4
	v_lshl_add_u64 v[2:3], v[2:3], 2, v[0:1]
	s_waitcnt lgkmcnt(0)
	global_store_dwordx4 v[2:3], v[6:9], off sc1
	ds_read_b128 v[2:5], v46 offset:1152
	s_nop 0
	v_or_b32_e32 v9, 0x50, v69
	v_mad_u64_u32 v[6:7], s[2:3], s0, v9, 0
	v_mov_b32_e32 v8, v7
	v_mad_u64_u32 v[8:9], s[2:3], s1, v9, v[8:9]
	v_mov_b32_e32 v7, v8
	v_lshl_add_u64 v[10:11], v[6:7], 2, v[0:1]
	ds_read_b128 v[6:9], v46 offset:2304
	s_waitcnt lgkmcnt(1)
	global_store_dwordx4 v[10:11], v[2:5], off sc1
	s_nop 1
	v_or_b32_e32 v5, 0x58, v69
	v_mad_u64_u32 v[2:3], s[2:3], s0, v5, 0
	v_mov_b32_e32 v4, v3
	v_mad_u64_u32 v[4:5], s[2:3], s1, v5, v[4:5]
	v_mov_b32_e32 v3, v4
	v_lshl_add_u64 v[2:3], v[2:3], 2, v[0:1]
	s_waitcnt lgkmcnt(0)
	global_store_dwordx4 v[2:3], v[6:9], off sc1
	ds_read_b128 v[2:5], v46 offset:3456
	s_nop 0
	v_or_b32_e32 v9, 0x60, v69
	v_mad_u64_u32 v[6:7], s[2:3], s0, v9, 0
	v_mov_b32_e32 v8, v7
	v_mad_u64_u32 v[8:9], s[2:3], s1, v9, v[8:9]
	v_mov_b32_e32 v7, v8
	v_lshl_add_u64 v[10:11], v[6:7], 2, v[0:1]
	ds_read_b128 v[6:9], v46 offset:4608
	s_waitcnt lgkmcnt(1)
	global_store_dwordx4 v[10:11], v[2:5], off sc1
	s_nop 1
	v_or_b32_e32 v5, 0x68, v69
	v_mad_u64_u32 v[2:3], s[2:3], s0, v5, 0
	v_mov_b32_e32 v4, v3
	v_mad_u64_u32 v[4:5], s[2:3], s1, v5, v[4:5]
	v_mov_b32_e32 v3, v4
	v_lshl_add_u64 v[2:3], v[2:3], 2, v[0:1]
	s_waitcnt lgkmcnt(0)
	global_store_dwordx4 v[2:3], v[6:9], off sc1
	ds_read_b128 v[2:5], v46 offset:5760
	s_nop 0
	v_or_b32_e32 v9, 0x70, v69
	v_mad_u64_u32 v[6:7], s[2:3], s0, v9, 0
	v_mov_b32_e32 v8, v7
	v_mad_u64_u32 v[8:9], s[2:3], s1, v9, v[8:9]
	v_mov_b32_e32 v7, v8
	v_lshl_add_u64 v[10:11], v[6:7], 2, v[0:1]
	ds_read_b128 v[6:9], v46 offset:6912
	s_waitcnt lgkmcnt(1)
	global_store_dwordx4 v[10:11], v[2:5], off sc1
	s_nop 1
	v_or_b32_e32 v5, 0x78, v69
	v_mad_u64_u32 v[2:3], s[2:3], s0, v5, 0
	v_mov_b32_e32 v4, v3
	v_mad_u64_u32 v[4:5], s[0:1], s1, v5, v[4:5]
	v_mov_b32_e32 v3, v4
	v_lshl_add_u64 v[0:1], v[2:3], 2, v[0:1]
	s_waitcnt lgkmcnt(0)
	global_store_dwordx4 v[0:1], v[6:9], off sc1
	s_endpgm
	s_endpgm
	s_endpgm
	s_endpgm
	s_endpgm
	s_endpgm
	s_endpgm
	s_endpgm
	s_endpgm
	s_endpgm
	s_endpgm
	s_endpgm
	s_endpgm
	s_endpgm
	s_endpgm
	s_endpgm
	s_endpgm
	s_endpgm
	s_endpgm
	s_endpgm
	s_endpgm
	s_endpgm
	s_endpgm
	s_endpgm
	s_endpgm
	s_endpgm
	s_endpgm
	s_endpgm
	s_endpgm
	s_endpgm
	s_endpgm
	s_endpgm
	s_endpgm
	s_endpgm
	s_endpgm
	s_endpgm
	s_endpgm
	s_endpgm
	s_endpgm
	s_endpgm
	s_endpgm
	s_endpgm
	s_endpgm
	s_endpgm
	s_endpgm
	s_endpgm
	.section	.rodata,"a",@progbits
	.p2align	6, 0x0

.LBB10_4:
	s_load_dwordx4 s[32:35], s[0:1], 0x18
	s_load_dword s36, s[0:1], 0x28
	s_load_dwordx4 s[4:7], s[0:1], 0x60
	s_load_dwordx2 s[12:13], s[0:1], 0x10
	s_ashr_i32 s2, s2, 3
	s_add_i32 s2, s3, s2
	s_abs_i32 s3, s2
	s_waitcnt lgkmcnt(0)
	s_lshl_b32 s26, s7, 6
	s_lshl_b32 s24, s26, 5
	s_mov_b32 s27, 0
	s_cmp_eq_u32 s12, 0x800
	s_cselect_b32 s25, s24, 32
	s_cselect_b32 s26, s26, 1
	s_cselect_b32 s12, 32, s12
	s_abs_i32 s14, s6
	v_cvt_f32_u32_e32 v1, s14
	s_sub_i32 s16, 0, s14
	s_xor_b32 s15, s2, s6
	s_ashr_i32 s15, s15, 31
	v_rcp_iflag_f32_e32 v1, v1
	v_lshlrev_b32_e32 v2, 3, v0
	v_lshrrev_b32_e32 v13, 2, v0
	v_and_b32_e32 v14, 24, v2
	v_mul_f32_e32 v1, 0x4f7ffffe, v1
	v_cvt_u32_f32_e32 v1, v1
	v_mov_b32_e32 v15, 0
	v_lshrrev_b32_e32 v11, 6, v0
	v_and_b32_e32 v10, 31, v0
	v_readfirstlane_b32 s17, v1
	s_mul_i32 s16, s16, s17
	s_mul_hi_u32 s16, s17, s16
	s_add_i32 s17, s17, s16
	s_mul_hi_u32 s16, s3, s17
	s_mul_i32 s17, s16, s14
	s_sub_i32 s3, s3, s17
	s_add_i32 s18, s16, 1
	s_sub_i32 s17, s3, s14
	s_cmp_ge_u32 s3, s14
	s_cselect_b32 s16, s18, s16
	s_cselect_b32 s3, s17, s3
	s_add_i32 s17, s16, 1
	s_cmp_ge_u32 s3, s14
	s_cselect_b32 s3, s17, s16
	s_abs_i32 s16, s7
	v_cvt_f32_u32_e32 v1, s16
	s_xor_b32 s3, s3, s15
	s_sub_i32 s3, s3, s15
	s_mul_i32 s6, s3, s6
	v_rcp_iflag_f32_e32 v1, v1
	s_sub_i32 s17, 0, s16
	s_sub_i32 s14, s2, s6
	s_xor_b32 s15, s3, s7
	v_mul_f32_e32 v1, 0x4f7ffffe, v1
	v_cvt_u32_f32_e32 v1, v1
	s_ashr_i32 s2, s15, 31
	s_abs_i32 s18, s3
	v_accvgpr_write_b32 a0, 0
	v_readfirstlane_b32 s6, v1
	s_mul_i32 s17, s17, s6
	s_mul_hi_u32 s15, s6, s17
	s_add_i32 s6, s6, s15
	s_mul_hi_u32 s6, s18, s6
	s_mul_i32 s15, s6, s16
	s_sub_i32 s15, s18, s15
	s_add_i32 s17, s6, 1
	s_sub_i32 s18, s15, s16
	s_cmp_ge_u32 s15, s16
	s_cselect_b32 s6, s17, s6
	s_cselect_b32 s15, s18, s15
	s_add_i32 s17, s6, 1
	s_cmp_ge_u32 s15, s16
	s_cselect_b32 s6, s17, s6
	s_xor_b32 s6, s6, s2
	s_sub_i32 s16, s6, s2
	s_mul_i32 s2, s16, s7
	s_sub_i32 s2, s3, s2
	s_lshl_b32 s15, s2, 6
	s_mul_i32 s2, s16, s4
	s_mul_i32 s26, s2, s26
	s_ashr_i32 s3, s2, 31
	v_or_b32_e32 v1, s15, v13
	s_ashr_i32 s17, s15, 31
	v_lshl_add_u64 v[2:3], s[26:27], 0, v[14:15]
	s_mul_i32 s18, s12, s17
	v_mad_u64_u32 v[2:3], s[6:7], s12, v1, v[2:3]
	v_mul_lo_u32 v1, s13, v1
	v_add3_u32 v3, v1, v3, s18
	v_lshlrev_b64 v[4:5], 1, v[2:3]
	v_lshl_add_u64 v[2:3], s[10:11], 0, v[4:5]
	v_lshl_add_u64 v[4:5], s[8:9], 0, v[4:5]
	global_load_dwordx4 v[76:79], v[4:5], off
	global_load_dwordx4 v[88:91], v[2:3], off
	s_load_dwordx2 s[6:7], s[0:1], 0x38
	s_movk_i32 s9, 0x50
	v_lshlrev_b32_e32 v14, 1, v14
	v_and_b32_e32 v1, 63, v0
	v_accvgpr_write_b32 a1, 0
	v_accvgpr_write_b32 a2, 0
	v_accvgpr_write_b32 a3, 0
	v_accvgpr_write_b32 a4, 0
	v_accvgpr_write_b32 a5, 0
	v_accvgpr_write_b32 a6, 0
	v_accvgpr_write_b32 a7, 0
	v_accvgpr_write_b32 a8, 0
	v_accvgpr_write_b32 a9, 0
	v_accvgpr_write_b32 a10, 0
	v_accvgpr_write_b32 a11, 0
	v_accvgpr_write_b32 a12, 0
	v_accvgpr_write_b32 a13, 0
	v_accvgpr_write_b32 a14, 0
	v_accvgpr_write_b32 a15, 0
	v_accvgpr_write_b32 a16, 0
	v_accvgpr_write_b32 a17, 0
	v_accvgpr_write_b32 a18, 0
	v_accvgpr_write_b32 a19, 0
	v_accvgpr_write_b32 a20, 0
	v_accvgpr_write_b32 a21, 0
	v_accvgpr_write_b32 a22, 0
	v_accvgpr_write_b32 a23, 0
	v_accvgpr_write_b32 a24, 0
	v_accvgpr_write_b32 a25, 0
	v_accvgpr_write_b32 a26, 0
	v_accvgpr_write_b32 a27, 0
	v_accvgpr_write_b32 a28, 0
	v_accvgpr_write_b32 a29, 0
	v_accvgpr_write_b32 a30, 0
	v_accvgpr_write_b32 a31, 0
	v_bfe_u32 v12, v0, 5, 1
	v_mad_u32_u24 v15, v13, s9, v14
	s_mov_b32 s10, s36
	s_lshr_b32 s3, s3, 28
	s_add_i32 s2, s2, s3
	s_ashr_i32 s2, s2, 4
	s_ashr_i32 s8, s4, 31
	s_waitcnt lgkmcnt(0)
	s_ashr_i32 s12, s10, 31
	s_lshr_b32 s12, s12, 28
	s_add_i32 s10, s10, s12
	s_ashr_i32 s3, s2, 31
	s_lshr_b32 s8, s8, 27
	v_lshl_or_b32 v8, s14, 2, v11
	s_ashr_i32 s10, s10, 4
	v_mov_b32_e32 v6, s2
	v_mov_b32_e32 v7, s3
	s_add_i32 s4, s4, s8
	v_mad_i64_i32 v[6:7], s[2:3], v8, s10, v[6:7]
	s_ashr_i32 s4, s4, 5
	v_lshlrev_b64 v[8:9], 10, v[6:7]
	s_add_i32 s8, s4, -1
	v_lshl_or_b32 v8, v1, 4, v8
	s_min_i32 s11, s8, 2
	v_lshl_add_u64 v[6:7], s[32:33], 0, v[8:9]
	s_lshl_b32 s28, s25, 1
	s_mov_b32 s29, 0
	v_lshl_add_u64 v[72:73], v[4:5], 0, s[28:29]
	v_lshl_add_u64 v[74:75], v[2:3], 0, s[28:29]
	global_load_dwordx4 v[28:31], v[72:73], off
	global_load_dwordx4 v[20:23], v[74:75], off
	v_lshl_add_u64 v[8:9], s[34:35], 0, v[8:9]
	global_load_dwordx4 v[36:39], v[6:7], off
	global_load_dwordx4 v[16:19], v[6:7], off offset:1024
	global_load_dwordx4 v[52:55], v[8:9], off
	global_load_dwordx4 v[24:27], v[8:9], off offset:1024
	global_load_dwordx4 v[40:43], v[6:7], off offset:2048
	global_load_dwordx4 v[48:51], v[8:9], off offset:2048
	s_mul_i32 s2, s11, s25
	s_ashr_i32 s3, s2, 31
	s_lshl_b64 s[2:3], s[2:3], 1
	v_lshl_add_u64 v[58:59], v[4:5], 0, s[2:3]
	v_lshl_add_u64 v[56:57], v[2:3], 0, s[2:3]
	global_load_dwordx4 v[44:47], v[58:59], off
	global_load_dwordx4 v[32:35], v[56:57], off
	s_waitcnt vmcnt(11)
	ds_write_b128 v15, v[76:79]
	s_waitcnt vmcnt(10)
	ds_write_b128 v15, v[88:91] offset:5120
	s_waitcnt lgkmcnt(0)
	s_barrier
	v_mul_u32_u24_e32 v15, 0x50, v13
	v_lshlrev_b32_e32 v13, 4, v12
	v_mad_u32_u24 v68, v10, s9, v13
	ds_read_b128 v[56:59], v68 offset:2560
	ds_read_b128 v[64:67], v68
	ds_read_b128 v[60:63], v68 offset:7680
	ds_read_b128 v[68:71], v68 offset:5120
	v_mul_u32_u24_e32 v72, 0x50, v10
	s_mov_b32 s2, 4
	v_accvgpr_write_b32 a31, 0
	v_accvgpr_write_b32 a30, 0
	v_accvgpr_write_b32 a29, 0
	v_accvgpr_write_b32 a28, 0
	v_accvgpr_write_b32 a27, 0
	v_accvgpr_write_b32 a26, 0
	v_accvgpr_write_b32 a25, 0
	v_accvgpr_write_b32 a24, 0
	v_accvgpr_write_b32 a23, 0
	v_accvgpr_write_b32 a22, 0
	v_accvgpr_write_b32 a21, 0
	v_accvgpr_write_b32 a20, 0
	v_accvgpr_write_b32 a19, 0
	v_accvgpr_write_b32 a18, 0
	v_accvgpr_write_b32 a17, 0
	v_accvgpr_write_b32 a16, 0
	v_accvgpr_write_b32 a15, 0
	v_accvgpr_write_b32 a14, 0
	v_accvgpr_write_b32 a13, 0
	v_accvgpr_write_b32 a12, 0
	v_accvgpr_write_b32 a11, 0
	v_accvgpr_write_b32 a10, 0
	v_accvgpr_write_b32 a9, 0
	v_accvgpr_write_b32 a8, 0
	v_accvgpr_write_b32 a7, 0
	v_accvgpr_write_b32 a6, 0
	v_accvgpr_write_b32 a5, 0
	v_accvgpr_write_b32 a4, 0
	v_accvgpr_write_b32 a3, 0
	v_accvgpr_write_b32 a2, 0
	v_accvgpr_write_b32 a1, 0
	v_accvgpr_write_b32 a0, 0
	v_add_u32_e32 v13, v13, v72
	v_add_u32_e32 v14, v14, v15
.LBB10_6:
	s_waitcnt vmcnt(7) lgkmcnt(0)
	v_mfma_f32_32x32x16_f16 a[0:15], v[68:71], v[36:39], a[0:15]
	s_add_i32 s3, s2, -3
	s_min_i32 s3, s3, s8
	s_lshl_b32 s3, s3, 1
	ds_read_b128 v[72:75], v13 offset:5152
	s_or_b32 s10, s3, 1
	s_ashr_i32 s11, s10, 31
	s_lshl_b64 s[10:11], s[10:11], 10
	v_lshl_add_u64 v[88:89], v[6:7], 0, s[10:11]
	v_lshl_add_u64 v[90:91], v[8:9], 0, s[10:11]
	s_waitcnt vmcnt(5)
	v_mfma_f32_32x32x16_f16 a[0:15], v[64:67], v[52:55], a[0:15]
	ds_read_b128 v[68:71], v13 offset:32
	v_mfma_f32_32x32x16_f16 a[0:15], v[64:67], v[36:39], a[0:15]
	ds_read_b128 v[76:79], v13 offset:7712
	ds_write_b128 v14, v[28:31] offset:10240
	global_load_dwordx4 v[80:83], v[88:89], off
	global_load_dwordx4 v[84:87], v[90:91], off
	v_mfma_f32_32x32x16_f16 a[16:31], v[60:63], v[36:39], a[16:31]
	ds_read_b128 v[64:67], v13 offset:2592
	ds_write_b128 v14, v[20:23] offset:15360
	v_mfma_f32_32x32x16_f16 a[16:31], v[56:59], v[52:55], a[16:31]
	v_mfma_f32_32x32x16_f16 a[16:31], v[56:59], v[36:39], a[16:31]
	s_add_i32 s3, s2, -1
	s_min_i32 s3, s3, s8
	s_mul_i32 s10, s3, s25
	s_ashr_i32 s11, s10, 31
	s_lshl_b64 s[10:11], s[10:11], 1
	v_lshl_add_u64 v[20:21], v[4:5], 0, s[10:11]
	s_waitcnt lgkmcnt(0)
	s_barrier
	global_load_dwordx4 v[28:31], v[20:21], off
	v_mfma_f32_32x32x16_f16 a[0:15], v[72:75], v[16:19], a[0:15]
	s_add_i32 s9, s2, -2
	ds_read_b128 v[56:59], v13 offset:15360
	v_lshl_add_u64 v[20:21], v[2:3], 0, s[10:11]
	s_min_i32 s10, s9, s8
	s_lshl_b32 s10, s10, 1
	s_ashr_i32 s11, s10, 31
	s_lshl_b64 s[12:13], s[10:11], 10
	v_lshl_add_u64 v[88:89], v[6:7], 0, s[12:13]
	v_lshl_add_u64 v[90:91], v[8:9], 0, s[12:13]
	global_load_dwordx4 v[20:23], v[20:21], off
	s_waitcnt vmcnt(8)
	v_mfma_f32_32x32x16_f16 a[0:15], v[68:71], v[24:27], a[0:15]
	ds_read_b128 v[60:63], v13 offset:10240
	v_mfma_f32_32x32x16_f16 a[0:15], v[68:71], v[16:19], a[0:15]
	ds_read_b128 v[72:75], v13 offset:17920
	global_load_dwordx4 v[36:39], v[88:89], off
	global_load_dwordx4 v[52:55], v[90:91], off
	v_mfma_f32_32x32x16_f16 a[16:31], v[76:79], v[16:19], a[16:31]
	ds_read_b128 v[68:71], v13 offset:12800
	v_mfma_f32_32x32x16_f16 a[16:31], v[64:67], v[24:27], a[16:31]
	v_mfma_f32_32x32x16_f16 a[16:31], v[64:67], v[16:19], a[16:31]
	s_waitcnt vmcnt(7) lgkmcnt(3)
	v_mfma_f32_32x32x16_f16 a[0:15], v[56:59], v[40:43], a[0:15]
	ds_read_b128 v[64:67], v13 offset:15392
	s_or_b32 s10, s10, 1
	s_ashr_i32 s11, s10, 31
	s_lshl_b64 s[10:11], s[10:11], 10
	v_lshl_add_u64 v[88:89], v[6:7], 0, s[10:11]
	v_lshl_add_u64 v[90:91], v[8:9], 0, s[10:11]
	s_waitcnt vmcnt(6) lgkmcnt(3)
	v_mfma_f32_32x32x16_f16 a[0:15], v[60:63], v[48:51], a[0:15]
	ds_read_b128 v[56:59], v13 offset:10272
	v_mfma_f32_32x32x16_f16 a[0:15], v[60:63], v[40:43], a[0:15]
	ds_read_b128 v[76:79], v13 offset:17952
	s_waitcnt vmcnt(7)
	ds_write_b128 v14, v[44:47]
	global_load_dwordx4 v[16:19], v[88:89], off
	global_load_dwordx4 v[24:27], v[90:91], off
	s_waitcnt lgkmcnt(5)
	v_mfma_f32_32x32x16_f16 a[16:31], v[72:75], v[40:43], a[16:31]
	ds_read_b128 v[88:91], v13 offset:12832
	s_waitcnt vmcnt(8)
	ds_write_b128 v14, v[32:35] offset:5120
	s_waitcnt lgkmcnt(6)
	v_mfma_f32_32x32x16_f16 a[16:31], v[68:71], v[48:51], a[16:31]
	v_mfma_f32_32x32x16_f16 a[16:31], v[68:71], v[40:43], a[16:31]
	s_min_i32 s10, s2, s8
	s_mul_i32 s10, s10, s25
	s_ashr_i32 s11, s10, 31
	s_lshl_b64 s[10:11], s[10:11], 1
	v_lshl_add_u64 v[32:33], v[4:5], 0, s[10:11]
	s_waitcnt lgkmcnt(0)
	s_barrier
	global_load_dwordx4 v[44:47], v[32:33], off
	s_waitcnt vmcnt(8)
	v_mfma_f32_32x32x16_f16 a[0:15], v[64:67], v[80:83], a[0:15]
	ds_read_b128 v[68:71], v13 offset:5120
	v_lshl_add_u64 v[32:33], v[2:3], 0, s[10:11]
	s_lshl_b32 s10, s3, 1
	s_ashr_i32 s11, s10, 31
	s_lshl_b64 s[10:11], s[10:11], 10
	v_lshl_add_u64 v[72:73], v[6:7], 0, s[10:11]
	v_lshl_add_u64 v[74:75], v[8:9], 0, s[10:11]
	global_load_dwordx4 v[32:35], v[32:33], off
	s_waitcnt vmcnt(8)
	v_mfma_f32_32x32x16_f16 a[0:15], v[56:59], v[84:87], a[0:15]
	ds_read_b128 v[64:67], v13
	v_mfma_f32_32x32x16_f16 a[0:15], v[56:59], v[80:83], a[0:15]
	ds_read_b128 v[60:63], v13 offset:7680
	global_load_dwordx4 v[40:43], v[72:73], off
	global_load_dwordx4 v[48:51], v[74:75], off
	v_mfma_f32_32x32x16_f16 a[16:31], v[76:79], v[80:83], a[16:31]
	ds_read_b128 v[56:59], v13 offset:2560
	v_mfma_f32_32x32x16_f16 a[16:31], v[88:91], v[84:87], a[16:31]
	v_mfma_f32_32x32x16_f16 a[16:31], v[88:91], v[80:83], a[16:31]
	s_add_i32 s2, s2, 2
	s_cmp_lt_i32 s9, s4
	s_cbranch_scc1 .LBB10_6
.LBB10_7:
	s_load_dwordx4 s[0:3], s[0:1], 0x40
	s_ashr_i32 s4, s16, 31
	s_waitcnt vmcnt(7)
	v_lshlrev_b32_e32 v37, 5, v11
	v_lshl_or_b32 v38, s14, 7, v37
	v_mul_u32_u24_e32 v37, 0x2400, v11
	s_waitcnt lgkmcnt(0)
	s_mul_hi_u32 s8, s2, s16
	s_mul_i32 s4, s2, s4
	s_add_i32 s4, s8, s4
	s_mul_i32 s3, s3, s16
	s_add_i32 s3, s4, s3
	s_mul_hi_u32 s4, s0, s15
	s_mul_i32 s8, s0, s17
	s_add_i32 s4, s4, s8
	s_mul_i32 s8, s1, s15
	v_accvgpr_read_b32 v36, a0
	s_waitcnt vmcnt(2)
	v_accvgpr_read_b32 v35, a1
	s_add_i32 s9, s4, s8
	v_lshl_or_b32 v10, v10, 2, v37
	s_movk_i32 s4, 0x240
	v_accvgpr_read_b32 v34, a2
	v_accvgpr_read_b32 v33, a3
	v_fma_f32 v36, s5, v36, 0
	v_mad_u32_u24 v10, v12, s4, v10
	v_fma_f32 v12, s5, v35, 0
	v_accvgpr_read_b32 v32, a4
	v_accvgpr_read_b32 v31, a5
	s_barrier
	ds_write2_b32 v10, v36, v12 offset1:36
	v_fma_f32 v12, s5, v34, 0
	v_fma_f32 v33, s5, v33, 0
	v_accvgpr_read_b32 v30, a6
	v_accvgpr_read_b32 v29, a7
	ds_write2_b32 v10, v12, v33 offset0:72 offset1:108
	v_fma_f32 v12, s5, v32, 0
	v_fma_f32 v31, s5, v31, 0
	v_add_u32_e32 v32, 0x400, v10
	v_accvgpr_read_b32 v28, a8
	v_accvgpr_read_b32 v27, a9
	ds_write2_b32 v32, v12, v31 offset0:32 offset1:68
	v_fma_f32 v12, s5, v30, 0
	v_fma_f32 v29, s5, v29, 0
	v_accvgpr_read_b32 v26, a10
	v_accvgpr_read_b32 v25, a11
	ds_write2_b32 v32, v12, v29 offset0:104 offset1:140
	v_fma_f32 v12, s5, v28, 0
	v_fma_f32 v27, s5, v27, 0
	v_add_u32_e32 v28, 0x800, v10
	v_accvgpr_read_b32 v24, a12
	v_accvgpr_read_b32 v23, a13
	ds_write2_b32 v28, v12, v27 offset0:64 offset1:100
	v_fma_f32 v12, s5, v26, 0
	v_fma_f32 v25, s5, v25, 0
	v_accvgpr_read_b32 v22, a14
	v_accvgpr_read_b32 v21, a15
	ds_write2_b32 v28, v12, v25 offset0:136 offset1:172
	v_fma_f32 v12, s5, v24, 0
	v_fma_f32 v23, s5, v23, 0
	v_add_u32_e32 v24, 0xc00, v10
	v_accvgpr_read_b32 v20, a16
	v_accvgpr_read_b32 v19, a17
	ds_write2_b32 v24, v12, v23 offset0:96 offset1:132
	v_fma_f32 v12, s5, v22, 0
	v_fma_f32 v21, s5, v21, 0
	v_accvgpr_read_b32 v18, a18
	v_accvgpr_read_b32 v17, a19
	ds_write2_b32 v24, v12, v21 offset0:168 offset1:204
	v_fma_f32 v12, s5, v20, 0
	v_fma_f32 v19, s5, v19, 0
	v_add_u32_e32 v20, 0x1000, v10
	v_accvgpr_read_b32 v16, a20
	v_accvgpr_read_b32 v15, a21
	ds_write2_b32 v20, v12, v19 offset0:128 offset1:164
	v_fma_f32 v12, s5, v18, 0
	v_fma_f32 v17, s5, v17, 0
	v_accvgpr_read_b32 v14, a22
	v_accvgpr_read_b32 v13, a23
	s_mul_i32 s2, s2, s16
	ds_write2_b32 v20, v12, v17 offset0:200 offset1:236
	v_fma_f32 v12, s5, v16, 0
	v_fma_f32 v15, s5, v15, 0
	v_add_u32_e32 v16, 0x1400, v10
	v_accvgpr_read_b32 v9, a24
	v_accvgpr_read_b32 v8, a25
	ds_write2_b32 v16, v12, v15 offset0:160 offset1:196
	v_fma_f32 v12, s5, v14, 0
	v_fma_f32 v13, s5, v13, 0
	v_add_u32_e32 v14, 0x1600, v10
	s_lshl_b64 s[2:3], s[2:3], 2
	v_accvgpr_read_b32 v7, a26
	v_accvgpr_read_b32 v6, a27
	v_accvgpr_read_b32 v5, a28
	v_accvgpr_read_b32 v4, a29
	v_accvgpr_read_b32 v3, a30
	v_accvgpr_read_b32 v2, a31
	s_mul_i32 s8, s0, s15
	ds_write2_b32 v14, v12, v13 offset0:104 offset1:140
	v_fma_f32 v9, s5, v9, 0
	v_fma_f32 v8, s5, v8, 0
	v_add_u32_e32 v12, 0x1800, v10
	s_add_u32 s4, s6, s2
	ds_write2_b32 v12, v9, v8 offset0:192 offset1:228
	v_fma_f32 v7, s5, v7, 0
	v_fma_f32 v6, s5, v6, 0
	v_add_u32_e32 v8, 0x1c00, v10
	v_fma_f32 v5, s5, v5, 0
	v_fma_f32 v4, s5, v4, 0
	v_fma_f32 v3, s5, v3, 0
	v_fma_f32 v2, s5, v2, 0
	s_addc_u32 s5, s7, s3
	s_lshl_b64 s[2:3], s[8:9], 2
	ds_write2_b32 v8, v7, v6 offset0:8 offset1:44
	v_add_u32_e32 v6, 0x1e00, v10
	s_add_u32 s2, s4, s2
	v_lshlrev_b32_e32 v0, 4, v0
	v_ashrrev_i32_e32 v39, 31, v38
	ds_write2_b32 v6, v5, v4 offset0:96 offset1:132
	v_add_u32_e32 v4, 0x2000, v10
	s_addc_u32 s3, s5, s3
	v_and_b32_e32 v10, 0x70, v0
	ds_write2_b32 v4, v3, v2 offset0:40 offset1:76
	v_lshrrev_b32_e32 v12, 3, v1
	v_lshl_add_u64 v[2:3], v[38:39], 2, s[2:3]
	v_or_b32_e32 v0, v37, v10
	s_movk_i32 s2, 0x90
	v_mov_b32_e32 v11, 0
	v_mad_u32_u24 v13, v12, s2, v0
	v_lshl_add_u64 v[8:9], v[2:3], 0, v[10:11]
	ds_read_b128 v[0:3], v13
	v_mad_u64_u32 v[4:5], s[2:3], s0, v12, 0
	v_mov_b32_e32 v6, v5
	v_mad_u64_u32 v[6:7], s[2:3], s1, v12, v[6:7]
	v_mov_b32_e32 v5, v6
	v_lshl_add_u64 v[10:11], v[4:5], 2, v[8:9]
	ds_read_b128 v[4:7], v13 offset:1152
	s_waitcnt lgkmcnt(1)
	global_store_dwordx4 v[10:11], v[0:3], off sc1
	s_nop 1
	v_or_b32_e32 v3, 8, v12
	v_mad_u64_u32 v[0:1], s[2:3], s0, v3, 0
	v_mov_b32_e32 v2, v1
	v_mad_u64_u32 v[2:3], s[2:3], s1, v3, v[2:3]
	v_mov_b32_e32 v1, v2
	v_lshl_add_u64 v[0:1], v[0:1], 2, v[8:9]
	s_waitcnt lgkmcnt(0)
	global_store_dwordx4 v[0:1], v[4:7], off sc1
	ds_read_b128 v[0:3], v13 offset:2304
	s_nop 0
	v_or_b32_e32 v7, 16, v12
	v_mad_u64_u32 v[4:5], s[2:3], s0, v7, 0
	v_mov_b32_e32 v6, v5
	v_mad_u64_u32 v[6:7], s[2:3], s1, v7, v[6:7]
	v_mov_b32_e32 v5, v6
	v_lshl_add_u64 v[10:11], v[4:5], 2, v[8:9]
	ds_read_b128 v[4:7], v13 offset:3456
	s_waitcnt lgkmcnt(1)
	global_store_dwordx4 v[10:11], v[0:3], off sc1
	s_nop 1
	v_or_b32_e32 v3, 24, v12
	v_mad_u64_u32 v[0:1], s[2:3], s0, v3, 0
	v_mov_b32_e32 v2, v1
	v_mad_u64_u32 v[2:3], s[2:3], s1, v3, v[2:3]
	v_mov_b32_e32 v1, v2
	v_lshl_add_u64 v[0:1], v[0:1], 2, v[8:9]
	s_waitcnt lgkmcnt(0)
	global_store_dwordx4 v[0:1], v[4:7], off sc1
	ds_read_b128 v[0:3], v13 offset:4608
	s_nop 0
	v_or_b32_e32 v7, 32, v12
	v_mad_u64_u32 v[4:5], s[2:3], s0, v7, 0
	v_mov_b32_e32 v6, v5
	v_mad_u64_u32 v[6:7], s[2:3], s1, v7, v[6:7]
	v_mov_b32_e32 v5, v6
	v_lshl_add_u64 v[10:11], v[4:5], 2, v[8:9]
	ds_read_b128 v[4:7], v13 offset:5760
	s_waitcnt lgkmcnt(1)
	global_store_dwordx4 v[10:11], v[0:3], off sc1
	s_nop 1
	v_or_b32_e32 v3, 40, v12
	v_mad_u64_u32 v[0:1], s[2:3], s0, v3, 0
	v_mov_b32_e32 v2, v1
	v_mad_u64_u32 v[2:3], s[2:3], s1, v3, v[2:3]
	v_mov_b32_e32 v1, v2
	v_lshl_add_u64 v[0:1], v[0:1], 2, v[8:9]
	s_waitcnt lgkmcnt(0)
	global_store_dwordx4 v[0:1], v[4:7], off sc1
	ds_read_b128 v[0:3], v13 offset:6912
	s_nop 0
	v_or_b32_e32 v7, 48, v12
	v_mad_u64_u32 v[4:5], s[2:3], s0, v7, 0
	v_mov_b32_e32 v6, v5
	v_mad_u64_u32 v[6:7], s[2:3], s1, v7, v[6:7]
	v_mov_b32_e32 v5, v6
	v_lshl_add_u64 v[10:11], v[4:5], 2, v[8:9]
	ds_read_b128 v[4:7], v13 offset:8064
	s_waitcnt lgkmcnt(1)
	global_store_dwordx4 v[10:11], v[0:3], off sc1
	s_nop 1
	v_or_b32_e32 v3, 56, v12
	v_mad_u64_u32 v[0:1], s[2:3], s0, v3, 0
	v_mov_b32_e32 v2, v1
	v_mad_u64_u32 v[2:3], s[0:1], s1, v3, v[2:3]
	v_mov_b32_e32 v1, v2
	v_lshl_add_u64 v[0:1], v[0:1], 2, v[8:9]
	s_waitcnt lgkmcnt(0)
	global_store_dwordx4 v[0:1], v[4:7], off sc1
	s_endpgm
	s_endpgm
	s_endpgm
	s_endpgm
	s_endpgm
	s_endpgm
	s_endpgm
	s_endpgm
	s_endpgm
	s_endpgm
	s_endpgm
	s_endpgm
	s_endpgm
	s_endpgm
	s_endpgm
	.section	.rodata,"a",@progbits
	.p2align	6, 0x0

.LBB11_4:
	s_load_dwordx4 s[4:7], s[0:1], 0x60
	s_load_dword s16, s[0:1], 0x70
	s_ashr_i32 s2, s2, 3
	s_add_i32 s18, s3, s2
	s_abs_i32 s2, s18
	s_waitcnt lgkmcnt(0)
	s_abs_i32 s17, s7
	v_cvt_f32_u32_e32 v1, s17
	s_xor_b32 s3, s18, s7
	s_ashr_i32 s19, s3, 31
	s_sub_i32 s3, 0, s17
	v_rcp_iflag_f32_e32 v1, v1
	v_lshrrev_b32_e32 v13, 2, v0
	v_mov_b32_e32 v31, 0
	v_lshrrev_b32_e32 v10, 1, v0
	v_mul_f32_e32 v1, 0x4f7ffffe, v1
	v_cvt_u32_f32_e32 v1, v1
	v_and_b32_e32 v11, 32, v13
	v_accvgpr_write_b32 a0, 0
	v_accvgpr_write_b32 a1, 0
	v_readfirstlane_b32 s20, v1
	s_mul_i32 s3, s3, s20
	s_mul_hi_u32 s3, s20, s3
	s_add_i32 s20, s20, s3
	s_mul_hi_u32 s3, s2, s20
	s_mul_i32 s20, s3, s17
	s_sub_i32 s2, s2, s20
	s_add_i32 s21, s3, 1
	s_sub_i32 s20, s2, s17
	s_cmp_ge_u32 s2, s17
	s_cselect_b32 s3, s21, s3
	s_cselect_b32 s2, s20, s2
	s_add_i32 s20, s3, 1
	s_cmp_ge_u32 s2, s17
	s_cselect_b32 s17, s20, s3
	s_abs_i32 s20, s16
	v_cvt_f32_u32_e32 v1, s20
	s_xor_b32 s17, s17, s19
	s_sub_i32 s19, s17, s19
	s_mul_i32 s7, s19, s7
	v_rcp_iflag_f32_e32 v1, v1
	s_xor_b32 s17, s19, s16
	s_sub_i32 s22, 0, s20
	s_sub_i32 s18, s18, s7
	v_mul_f32_e32 v1, 0x4f7ffffe, v1
	v_cvt_u32_f32_e32 v1, v1
	s_ashr_i32 s7, s17, 31
	s_abs_i32 s23, s19
	s_load_dwordx2 s[2:3], s[0:1], 0x10
	s_load_dword s21, s[0:1], 0x28
	v_readfirstlane_b32 s17, v1
	s_mul_i32 s22, s22, s17
	s_mul_hi_u32 s22, s17, s22
	s_add_i32 s17, s17, s22
	s_mul_hi_u32 s17, s23, s17
	s_mul_i32 s22, s17, s20
	s_sub_i32 s22, s23, s22
	s_add_i32 s24, s17, 1
	s_sub_i32 s23, s22, s20
	s_cmp_ge_u32 s22, s20
	s_cselect_b32 s17, s24, s17
	s_cselect_b32 s22, s23, s22
	s_add_i32 s23, s17, 1
	s_cmp_ge_u32 s22, s20
	s_cselect_b32 s17, s23, s17
	s_xor_b32 s17, s17, s7
	s_sub_i32 s17, s17, s7
	s_mul_i32 s7, s17, s16
	s_lshl_b32 s16, s18, 6
	v_lshlrev_b32_e32 v1, 3, v0
	s_mul_i32 s18, s17, s5
	s_sub_i32 s7, s19, s7
	v_and_b32_e32 v30, 24, v1
	s_ashr_i32 s19, s18, 31
	s_lshl_b32 s7, s7, 6
	v_lshl_add_u64 v[2:3], s[18:19], 0, v[30:31]
	v_or_b32_e32 v4, s16, v13
	s_add_i32 s18, s4, -1
	v_or_b32_e32 v1, s7, v13
	s_ashr_i32 s20, s7, 31
	v_min_i32_e32 v6, s18, v4
	s_waitcnt lgkmcnt(0)
	s_mul_i32 s20, s2, s20
	v_mad_u64_u32 v[4:5], s[18:19], s2, v1, v[2:3]
	v_mul_lo_u32 v1, s3, v1
	v_mad_i64_i32 v[6:7], s[2:3], v6, s21, v[2:3]
	v_add3_u32 v5, v1, v5, s20
	v_lshlrev_b64 v[6:7], 1, v[6:7]
	v_lshlrev_b64 v[8:9], 1, v[4:5]
	v_lshl_add_u64 v[4:5], s[12:13], 0, v[6:7]
	global_load_dwordx4 v[64:67], v[4:5], off
	v_lshl_add_u64 v[6:7], s[14:15], 0, v[6:7]
	v_lshl_add_u64 v[2:3], s[8:9], 0, v[8:9]
	global_load_dwordx4 v[68:71], v[6:7], off
	global_load_dwordx4 v[72:75], v[2:3], off
	v_lshl_add_u64 v[8:9], s[10:11], 0, v[8:9]
	global_load_dwordx4 v[76:79], v[8:9], off
	s_load_dwordx2 s[8:9], s[0:1], 0x38
	v_mul_u32_u24_e32 v13, 40, v13
	v_lshlrev_b32_e32 v30, 1, v30
	s_mov_b32 s2, 0
	v_and_b32_e32 v1, 31, v0
	v_accvgpr_write_b32 a2, 0
	v_accvgpr_write_b32 a3, 0
	v_accvgpr_write_b32 a4, 0
	v_accvgpr_write_b32 a5, 0
	v_accvgpr_write_b32 a6, 0
	v_accvgpr_write_b32 a7, 0
	v_accvgpr_write_b32 a8, 0
	v_accvgpr_write_b32 a9, 0
	v_accvgpr_write_b32 a10, 0
	v_accvgpr_write_b32 a11, 0
	v_accvgpr_write_b32 a12, 0
	v_accvgpr_write_b32 a13, 0
	v_accvgpr_write_b32 a14, 0
	v_accvgpr_write_b32 a15, 0
	v_bfe_u32 v12, v0, 5, 1
	v_and_b32_e32 v10, 32, v10
	v_lshl_add_u32 v13, v13, 1, v30
	s_ashr_i32 s3, s5, 31
	s_lshr_b32 s3, s3, 27
	s_add_i32 s3, s5, s3
	s_ashr_i32 s3, s3, 5
	s_add_i32 s5, s3, -1
	s_min_i32 s10, s5, 2
	s_lshl_b32 s10, s10, 5
	s_ashr_i32 s11, s10, 31
	s_lshl_b64 s[10:11], s[10:11], 1
	v_lshl_add_u64 v[14:15], v[2:3], 0, s[10:11]
	global_load_dwordx4 v[16:19], v[2:3], off offset:64
	global_load_dwordx4 v[20:23], v[8:9], off offset:64
	global_load_dwordx4 v[24:27], v[4:5], off offset:64
	global_load_dwordx4 v[32:35], v[6:7], off offset:64
	global_load_dwordx4 v[28:31], v[14:15], off
	v_lshl_add_u64 v[14:15], v[8:9], 0, s[10:11]
	global_load_dwordx4 v[36:39], v[14:15], off
	v_lshl_add_u64 v[14:15], v[4:5], 0, s[10:11]
	global_load_dwordx4 v[40:43], v[14:15], off
	v_lshl_add_u64 v[14:15], v[6:7], 0, s[10:11]
	global_load_dwordx4 v[44:47], v[14:15], off
	s_waitcnt vmcnt(11)
	ds_write_b128 v13, v[64:67] offset:10240
	s_waitcnt vmcnt(10)
	ds_write_b128 v13, v[68:71] offset:15360
	s_waitcnt vmcnt(9)
	ds_write_b128 v13, v[72:75]
	s_waitcnt vmcnt(8)
	ds_write_b128 v13, v[76:79] offset:5120
	s_waitcnt lgkmcnt(0)
	s_barrier
	v_or_b32_e32 v15, v10, v1
	v_lshlrev_b32_e32 v64, 4, v12
	s_movk_i32 s10, 0x50
	v_or_b32_e32 v14, v11, v1
	v_mul_u32_u24_e32 v65, 0x50, v15
	v_mad_u32_u24 v15, v15, s10, v64
	v_mul_u32_u24_e32 v66, 0x50, v14
	v_mad_u32_u24 v14, v14, s10, v64
	ds_read_b128 v[56:59], v15 offset:15360
	ds_read_b128 v[48:51], v15 offset:10240
	ds_read_b128 v[52:55], v14
	ds_read_b128 v[60:63], v14 offset:5120
	v_accvgpr_write_b32 a15, 0
	v_accvgpr_write_b32 a14, 0
	v_accvgpr_write_b32 a13, 0
	v_accvgpr_write_b32 a12, 0
	v_accvgpr_write_b32 a11, 0
	v_accvgpr_write_b32 a10, 0
	v_accvgpr_write_b32 a9, 0
	v_accvgpr_write_b32 a8, 0
	v_accvgpr_write_b32 a7, 0
	v_accvgpr_write_b32 a6, 0
	v_accvgpr_write_b32 a5, 0
	v_accvgpr_write_b32 a4, 0
	v_accvgpr_write_b32 a3, 0
	v_accvgpr_write_b32 a2, 0
	v_accvgpr_write_b32 a1, 0
	v_accvgpr_write_b32 a0, 0
	v_add_u32_e32 v14, v64, v66
	v_add_u32_e32 v15, v64, v65

.LBB11_7:
	v_lshrrev_b32_e32 v3, 6, v0
	v_mul_u32_u24_e32 v3, 0x1200, v3
	s_waitcnt vmcnt(6)
	s_nop 5
	v_accvgpr_read_b32 v20, a2
	v_accvgpr_read_b32 v19, a3
	v_lshl_or_b32 v23, v1, 2, v3
	s_movk_i32 s2, 0x240
	v_accvgpr_read_b32 v16, a6
	v_accvgpr_read_b32 v15, a7
	v_mad_u32_u24 v12, v12, s2, v23
	v_fma_f32 v20, s6, v20, 0
	v_fma_f32 v19, s6, v19, 0
	v_accvgpr_read_b32 v9, a10
	v_accvgpr_read_b32 v8, a11
	s_waitcnt lgkmcnt(0)
	s_barrier
	ds_write2_b32 v12, v20, v19 offset0:72 offset1:108
	v_add_u32_e32 v19, 0x400, v12
	v_fma_f32 v16, s6, v16, 0
	v_fma_f32 v15, s6, v15, 0
	v_and_b32_e32 v2, 63, v0
	v_accvgpr_read_b32 v5, a14
	v_accvgpr_read_b32 v4, a15
	ds_write2_b32 v19, v16, v15 offset0:104 offset1:140
	v_add_u32_e32 v15, 0x800, v12
	v_fma_f32 v9, s6, v9, 0
	v_fma_f32 v8, s6, v8, 0
	v_lshlrev_b32_e32 v0, 2, v0
	ds_write2_b32 v15, v9, v8 offset0:136 offset1:172
	v_add_u32_e32 v8, 0xc00, v12
	v_fma_f32 v5, s6, v5, 0
	v_fma_f32 v4, s6, v4, 0
	v_and_b32_e32 v0, 28, v0
	v_accvgpr_read_b32 v22, a0
	v_accvgpr_read_b32 v21, a1
	v_accvgpr_read_b32 v18, a4
	v_accvgpr_read_b32 v17, a5
	v_accvgpr_read_b32 v14, a8
	v_accvgpr_read_b32 v13, a9
	v_accvgpr_read_b32 v7, a12
	v_accvgpr_read_b32 v6, a13
	ds_write2_b32 v8, v5, v4 offset0:168 offset1:204
	v_or3_b32 v4, v10, v0, s16
	v_mov_b32_e32 v1, 0
	v_fma_f32 v22, s6, v22, 0
	v_fma_f32 v21, s6, v21, 0
	v_fma_f32 v18, s6, v18, 0
	v_fma_f32 v17, s6, v17, 0
	v_fma_f32 v14, s6, v14, 0
	v_fma_f32 v13, s6, v13, 0
	v_fma_f32 v7, s6, v7, 0
	v_fma_f32 v6, s6, v6, 0
	v_cmp_gt_i32_e32 vcc, s4, v4
	ds_write2_b32 v12, v22, v21 offset1:36
	ds_write2_b32 v19, v18, v17 offset0:32 offset1:68
	ds_write2_b32 v15, v14, v13 offset0:64 offset1:100
	ds_write2_b32 v8, v7, v6 offset0:96 offset1:132
	s_and_saveexec_b64 s[2:3], vcc
	s_cbranch_execz .LBB11_9
	s_load_dwordx4 s[0:3], s[0:1], 0x40
	s_ashr_i32 s4, s17, 31
	v_lshlrev_b32_e32 v4, 2, v0
	v_add_u32_e32 v0, s7, v11
	v_ashrrev_i32_e32 v5, 31, v0
	s_waitcnt lgkmcnt(0)
	s_mul_hi_u32 s5, s2, s17
	s_mul_i32 s4, s2, s4
	s_mul_i32 s3, s3, s17
	s_add_i32 s4, s5, s4
	s_add_i32 s3, s4, s3
	s_mul_i32 s2, s2, s17
	s_lshl_b64 s[2:3], s[2:3], 2
	s_add_u32 s2, s8, s2
	v_mul_lo_u32 v5, s0, v5
	v_mul_lo_u32 v8, s1, v0
	v_mad_u64_u32 v[6:7], s[4:5], s0, v0, 0
	s_addc_u32 s3, s9, s3
	v_add3_u32 v7, v7, v5, v8
	v_lshl_add_u64 v[6:7], v[6:7], 2, s[2:3]
	s_ashr_i32 s17, s16, 31
	v_lshl_add_u64 v[6:7], s[16:17], 2, v[6:7]
	v_lshlrev_b32_e32 v0, 2, v10
	v_lshrrev_b32_e32 v12, 3, v2
	v_lshl_add_u64 v[6:7], v[6:7], 0, v[0:1]
	v_mul_u32_u24_e32 v0, 0x90, v12
	v_mov_b32_e32 v5, v1
	v_add3_u32 v13, v3, v4, v0
	v_lshl_add_u64 v[8:9], v[6:7], 0, v[4:5]
	ds_read_b128 v[0:3], v13
	v_mad_u64_u32 v[4:5], s[2:3], s0, v12, 0
	v_mov_b32_e32 v6, v5
	v_mad_u64_u32 v[6:7], s[2:3], s1, v12, v[6:7]
	v_mov_b32_e32 v5, v6
	v_lshl_add_u64 v[10:11], v[4:5], 2, v[8:9]
	ds_read_b128 v[4:7], v13 offset:1152
	s_waitcnt lgkmcnt(1)
	global_store_dwordx4 v[10:11], v[0:3], off sc1
	s_nop 1
	v_or_b32_e32 v3, 8, v12
	v_mad_u64_u32 v[0:1], s[2:3], s0, v3, 0
	v_mov_b32_e32 v2, v1
	v_mad_u64_u32 v[2:3], s[2:3], s1, v3, v[2:3]
	v_mov_b32_e32 v1, v2
	v_lshl_add_u64 v[0:1], v[0:1], 2, v[8:9]
	s_waitcnt lgkmcnt(0)
	global_store_dwordx4 v[0:1], v[4:7], off sc1
	ds_read_b128 v[0:3], v13 offset:2304
	s_nop 0
	v_or_b32_e32 v7, 16, v12
	v_mad_u64_u32 v[4:5], s[2:3], s0, v7, 0
	v_mov_b32_e32 v6, v5
	v_mad_u64_u32 v[6:7], s[2:3], s1, v7, v[6:7]
	v_mov_b32_e32 v5, v6
	v_lshl_add_u64 v[10:11], v[4:5], 2, v[8:9]
	ds_read_b128 v[4:7], v13 offset:3456
	s_waitcnt lgkmcnt(1)
	global_store_dwordx4 v[10:11], v[0:3], off sc1
	s_nop 1
	v_or_b32_e32 v3, 24, v12
	v_mad_u64_u32 v[0:1], s[2:3], s0, v3, 0
	v_mov_b32_e32 v2, v1
	v_mad_u64_u32 v[2:3], s[0:1], s1, v3, v[2:3]
	v_mov_b32_e32 v1, v2
	v_lshl_add_u64 v[0:1], v[0:1], 2, v[8:9]
	s_waitcnt lgkmcnt(0)
	global_store_dwordx4 v[0:1], v[4:7], off sc1
.LBB11_9:
	s_endpgm
	s_endpgm
	s_endpgm
	s_endpgm
	s_endpgm
	s_endpgm
	s_endpgm
	s_endpgm
	s_endpgm
	s_endpgm
	s_endpgm
	s_endpgm
	s_endpgm
	s_endpgm
	s_endpgm
	s_endpgm
	s_endpgm
	s_endpgm
	s_endpgm
	.section	.rodata,"a",@progbits
	.p2align	6, 0x0

.LBB16_4:
	s_load_dwordx4 s[32:35], s[0:1], 0x18
	s_load_dword s36, s[0:1], 0x28
	s_load_dwordx4 s[4:7], s[0:1], 0x60
	s_load_dwordx2 s[14:15], s[0:1], 0x10
	s_ashr_i32 s2, s2, 3
	s_add_i32 s2, s3, s2
	s_abs_i32 s3, s2
	s_waitcnt lgkmcnt(0)
	s_abs_i32 s16, s6
	v_cvt_f32_u32_e32 v1, s16
	s_sub_i32 s18, 0, s16
	s_xor_b32 s17, s2, s6
	s_ashr_i32 s17, s17, 31
	v_rcp_iflag_f32_e32 v1, v1
	v_lshrrev_b32_e32 v11, 6, v0
	v_mov_b32_e32 v9, 0
	v_lshlrev_b32_e32 v6, 5, v11
	v_mul_f32_e32 v1, 0x4f7ffffe, v1
	v_cvt_u32_f32_e32 v1, v1
	v_and_b32_e32 v24, 31, v0
	v_and_b32_e32 v25, 63, v0
	v_bfe_u32 v26, v0, 5, 1
	v_readfirstlane_b32 s19, v1
	s_mul_i32 s18, s18, s19
	s_mul_hi_u32 s18, s19, s18
	s_add_i32 s19, s19, s18
	s_mul_hi_u32 s18, s3, s19
	s_mul_i32 s19, s18, s16
	s_sub_i32 s3, s3, s19
	s_add_i32 s20, s18, 1
	s_sub_i32 s19, s3, s16
	s_cmp_ge_u32 s3, s16
	s_cselect_b32 s18, s20, s18
	s_cselect_b32 s3, s19, s3
	s_add_i32 s19, s18, 1
	s_cmp_ge_u32 s3, s16
	s_cselect_b32 s3, s19, s18
	s_abs_i32 s18, s7
	v_cvt_f32_u32_e32 v2, s18
	s_xor_b32 s3, s3, s17
	s_sub_i32 s3, s3, s17
	s_mul_i32 s6, s3, s6
	v_rcp_iflag_f32_e32 v2, v2
	s_sub_i32 s19, 0, s18
	s_sub_i32 s16, s2, s6
	s_xor_b32 s17, s3, s7
	v_mul_f32_e32 v2, 0x4f7ffffe, v2
	v_cvt_u32_f32_e32 v2, v2
	s_ashr_i32 s2, s17, 31
	s_abs_i32 s20, s3
	v_lshrrev_b32_e32 v1, 2, v0
	v_readfirstlane_b32 s6, v2
	s_mul_i32 s19, s19, s6
	s_mul_hi_u32 s17, s6, s19
	s_add_i32 s6, s6, s17
	s_mul_hi_u32 s6, s20, s6
	s_mul_i32 s17, s6, s18
	s_sub_i32 s17, s20, s17
	s_add_i32 s19, s6, 1
	s_sub_i32 s20, s17, s18
	s_cmp_ge_u32 s17, s18
	s_cselect_b32 s6, s19, s6
	s_cselect_b32 s17, s20, s17
	s_add_i32 s19, s6, 1
	s_cmp_ge_u32 s17, s18
	s_cselect_b32 s6, s19, s6
	s_xor_b32 s6, s6, s2
	s_sub_i32 s2, s6, s2
	s_mul_i32 s6, s2, s7
	s_sub_i32 s3, s3, s6
	v_lshlrev_b32_e32 v2, 3, v0
	s_mul_i32 s2, s2, s4
	s_lshl_b32 s6, s3, 7
	v_and_b32_e32 v8, 24, v2
	s_ashr_i32 s3, s2, 31
	v_or_b32_e32 v4, s6, v1
	s_ashr_i32 s7, s6, 31
	v_lshl_add_u64 v[2:3], s[2:3], 0, v[8:9]
	s_mul_i32 s17, s14, s7
	v_mad_u64_u32 v[2:3], s[20:21], s14, v4, v[2:3]
	v_mul_lo_u32 v4, s15, v4
	v_lshl_or_b32 v10, s16, 7, v6
	s_lshl_b64 s[18:19], s[14:15], 6
	v_add3_u32 v3, v4, v3, s17
	v_or_b32_e32 v6, v10, v24
	v_lshl_add_u64 v[4:5], v[2:3], 0, s[18:19]
	v_lshlrev_b64 v[2:3], 1, v[2:3]
	v_ashrrev_i32_e32 v7, 31, v6
	v_lshl_add_u64 v[12:13], v[4:5], 1, s[10:11]
	v_lshl_add_u64 v[14:15], s[12:13], 0, v[2:3]
	v_lshl_add_u64 v[16:17], s[10:11], 0, v[2:3]
	s_lshl_b64 s[10:11], s[14:15], 7
	v_lshl_add_u64 v[6:7], v[6:7], 2, s[8:9]
	v_lshl_add_u64 v[18:19], v[14:15], 0, s[10:11]
	global_load_dwordx4 v[126:129], v[16:17], off
	global_load_dwordx4 v[130:133], v[14:15], off
	global_load_dwordx4 v[134:137], v[12:13], off
	global_load_dwordx4 v[138:141], v[18:19], off
	global_load_dword v9, v[6:7], off
	v_lshlrev_b32_e32 v0, 1, v8
	s_movk_i32 s9, 0x50
	v_accvgpr_write_b32 a48, 0
	v_accvgpr_write_b32 a49, 0
	v_accvgpr_write_b32 a50, 0
	v_accvgpr_write_b32 a51, 0
	v_accvgpr_write_b32 a52, 0
	v_accvgpr_write_b32 a53, 0
	v_accvgpr_write_b32 a54, 0
	v_accvgpr_write_b32 a55, 0
	v_accvgpr_write_b32 a56, 0
	v_accvgpr_write_b32 a57, 0
	v_accvgpr_write_b32 a58, 0
	v_accvgpr_write_b32 a59, 0
	v_accvgpr_write_b32 a60, 0
	v_accvgpr_write_b32 a61, 0
	v_accvgpr_write_b32 a62, 0
	v_accvgpr_write_b32 a63, 0
	v_accvgpr_write_b32 a32, 0
	v_accvgpr_write_b32 a33, 0
	v_accvgpr_write_b32 a34, 0
	v_accvgpr_write_b32 a35, 0
	v_accvgpr_write_b32 a36, 0
	v_accvgpr_write_b32 a37, 0
	v_accvgpr_write_b32 a38, 0
	v_accvgpr_write_b32 a39, 0
	v_accvgpr_write_b32 a40, 0
	v_accvgpr_write_b32 a41, 0
	v_accvgpr_write_b32 a42, 0
	v_accvgpr_write_b32 a43, 0
	v_accvgpr_write_b32 a44, 0
	v_accvgpr_write_b32 a45, 0
	v_accvgpr_write_b32 a46, 0
	v_accvgpr_write_b32 a47, 0
	v_accvgpr_write_b32 a16, 0
	v_accvgpr_write_b32 a17, 0
	v_accvgpr_write_b32 a18, 0
	v_accvgpr_write_b32 a19, 0
	v_accvgpr_write_b32 a20, 0
	v_accvgpr_write_b32 a21, 0
	v_accvgpr_write_b32 a22, 0
	v_accvgpr_write_b32 a23, 0
	v_accvgpr_write_b32 a24, 0
	v_accvgpr_write_b32 a25, 0
	v_accvgpr_write_b32 a26, 0
	v_accvgpr_write_b32 a27, 0
	v_accvgpr_write_b32 a28, 0
	v_accvgpr_write_b32 a29, 0
	v_accvgpr_write_b32 a30, 0
	v_accvgpr_write_b32 a31, 0
	v_accvgpr_write_b32 a0, 0
	v_accvgpr_write_b32 a1, 0
	v_accvgpr_write_b32 a2, 0
	v_accvgpr_write_b32 a3, 0
	v_accvgpr_write_b32 a4, 0
	v_accvgpr_write_b32 a5, 0
	v_accvgpr_write_b32 a6, 0
	v_accvgpr_write_b32 a7, 0
	v_accvgpr_write_b32 a8, 0
	v_accvgpr_write_b32 a9, 0
	v_accvgpr_write_b32 a10, 0
	v_accvgpr_write_b32 a11, 0
	v_accvgpr_write_b32 a12, 0
	v_accvgpr_write_b32 a13, 0
	v_accvgpr_write_b32 a14, 0
	v_accvgpr_write_b32 a15, 0
	v_mad_u32_u24 v118, v1, s9, v0
	s_mov_b32 s10, s36
	s_lshr_b32 s3, s3, 28
	s_ashr_i32 s8, s4, 31
	v_lshl_or_b32 v4, s16, 2, v11
	s_add_i32 s2, s2, s3
	s_waitcnt lgkmcnt(0)
	s_ashr_i32 s16, s10, 31
	s_lshr_b32 s8, s8, 27
	s_lshr_b32 s16, s16, 28
	s_ashr_i32 s2, s2, 4
	s_add_i32 s4, s4, s8
	s_add_i32 s10, s10, s16
	s_ashr_i32 s3, s2, 31
	s_ashr_i32 s4, s4, 5
	s_ashr_i32 s10, s10, 4
	v_mov_b32_e32 v2, s2
	v_mov_b32_e32 v3, s3
	s_add_i32 s8, s4, -1
	v_mad_i64_i32 v[2:3], s[2:3], v4, s10, v[2:3]
	s_min_i32 s11, s8, 2
	v_lshlrev_b64 v[2:3], 10, v[2:3]
	v_lshl_or_b32 v2, v25, 4, v2
	s_lshl_b32 s2, s11, 5
	v_lshl_add_u64 v[20:21], s[32:33], 0, v[2:3]
	s_ashr_i32 s3, s2, 31
	global_load_dwordx4 v[46:49], v[16:17], off offset:64
	global_load_dwordx4 v[50:53], v[14:15], off offset:64
	global_load_dwordx4 v[34:37], v[12:13], off offset:64
	global_load_dwordx4 v[30:33], v[18:19], off offset:64
	v_lshl_add_u64 v[22:23], s[34:35], 0, v[2:3]
	global_load_dwordx4 v[66:69], v[20:21], off
	global_load_dwordx4 v[38:41], v[20:21], off offset:1024
	global_load_dwordx4 v[82:85], v[22:23], off
	global_load_dwordx4 v[42:45], v[22:23], off offset:1024
	global_load_dwordx4 v[70:73], v[20:21], off offset:2048
	global_load_dwordx4 v[78:81], v[22:23], off offset:2048
	s_lshl_b64 s[2:3], s[2:3], 1
	v_lshl_add_u64 v[28:29], v[16:17], 0, s[2:3]
	v_lshl_add_u64 v[2:3], v[12:13], 0, s[2:3]
	v_lshl_add_u64 v[4:5], v[14:15], 0, s[2:3]
	v_lshl_add_u64 v[6:7], v[18:19], 0, s[2:3]
	global_load_dwordx4 v[62:65], v[28:29], off
	global_load_dwordx4 v[58:61], v[2:3], off
	global_load_dwordx4 v[74:77], v[4:5], off
	global_load_dwordx4 v[54:57], v[6:7], off
	s_waitcnt vmcnt(18)
	ds_write_b128 v118, v[126:129]
	s_waitcnt vmcnt(17)
	ds_write_b128 v118, v[130:133] offset:10240
	s_waitcnt vmcnt(16)
	ds_write_b128 v118, v[134:137] offset:5120
	s_waitcnt vmcnt(15)
	ds_write_b128 v118, v[138:141] offset:15360
	s_waitcnt lgkmcnt(0)
	s_barrier
	v_lshlrev_b32_e32 v2, 4, v26
	v_mad_u32_u24 v4, v24, s9, v2
	ds_read_b128 v[86:89], v4 offset:7680
	ds_read_b128 v[94:97], v4 offset:5120
	ds_read_b128 v[90:93], v4 offset:17920
	ds_read_b128 v[98:101], v4 offset:15360
	ds_read_b128 v[102:105], v4 offset:2560
	ds_read_b128 v[106:109], v4
	ds_read_b128 v[110:113], v4 offset:12800
	ds_read_b128 v[114:117], v4 offset:10240
	v_mul_u32_u24_e32 v1, 0x50, v1
	v_mul_u32_u24_e32 v3, 0x50, v24
	s_mov_b32 s2, 4
	v_accvgpr_write_b32 a15, 0
	v_accvgpr_write_b32 a14, 0
	v_accvgpr_write_b32 a13, 0
	v_accvgpr_write_b32 a12, 0
	v_accvgpr_write_b32 a11, 0
	v_accvgpr_write_b32 a10, 0
	v_accvgpr_write_b32 a9, 0
	v_accvgpr_write_b32 a8, 0
	v_accvgpr_write_b32 a7, 0
	v_accvgpr_write_b32 a6, 0
	v_accvgpr_write_b32 a5, 0
	v_accvgpr_write_b32 a4, 0
	v_accvgpr_write_b32 a3, 0
	v_accvgpr_write_b32 a2, 0
	v_accvgpr_write_b32 a1, 0
	v_accvgpr_write_b32 a0, 0
	v_accvgpr_write_b32 a31, 0
	v_accvgpr_write_b32 a30, 0
	v_accvgpr_write_b32 a29, 0
	v_accvgpr_write_b32 a28, 0
	v_accvgpr_write_b32 a27, 0
	v_accvgpr_write_b32 a26, 0
	v_accvgpr_write_b32 a25, 0
	v_accvgpr_write_b32 a24, 0
	v_accvgpr_write_b32 a23, 0
	v_accvgpr_write_b32 a22, 0
	v_accvgpr_write_b32 a21, 0
	v_accvgpr_write_b32 a20, 0
	v_accvgpr_write_b32 a19, 0
	v_accvgpr_write_b32 a18, 0
	v_accvgpr_write_b32 a17, 0
	v_accvgpr_write_b32 a16, 0
	v_accvgpr_write_b32 a47, 0
	v_accvgpr_write_b32 a46, 0
	v_accvgpr_write_b32 a45, 0
	v_accvgpr_write_b32 a44, 0
	v_accvgpr_write_b32 a43, 0
	v_accvgpr_write_b32 a42, 0
	v_accvgpr_write_b32 a41, 0
	v_accvgpr_write_b32 a40, 0
	v_accvgpr_write_b32 a39, 0
	v_accvgpr_write_b32 a38, 0
	v_accvgpr_write_b32 a37, 0
	v_accvgpr_write_b32 a36, 0
	v_accvgpr_write_b32 a35, 0
	v_accvgpr_write_b32 a34, 0
	v_accvgpr_write_b32 a33, 0
	v_accvgpr_write_b32 a32, 0
	v_accvgpr_write_b32 a63, 0
	v_accvgpr_write_b32 a62, 0
	v_accvgpr_write_b32 a61, 0
	v_accvgpr_write_b32 a60, 0
	v_accvgpr_write_b32 a59, 0
	v_accvgpr_write_b32 a58, 0
	v_accvgpr_write_b32 a57, 0
	v_accvgpr_write_b32 a56, 0
	v_accvgpr_write_b32 a55, 0
	v_accvgpr_write_b32 a54, 0
	v_accvgpr_write_b32 a53, 0
	v_accvgpr_write_b32 a52, 0
	v_accvgpr_write_b32 a51, 0
	v_accvgpr_write_b32 a50, 0
	v_accvgpr_write_b32 a49, 0
	v_accvgpr_write_b32 a48, 0
	v_add_u32_e32 v27, v2, v3
	v_add_u32_e32 v28, v0, v1

.LBB16_7:
	s_load_dwordx4 s[8:11], s[0:1], 0x50
	s_waitcnt vmcnt(4)
	v_mul_u32_u24_e32 v76, 0x2800, v11
	s_load_dword s24, s[0:1], 0x6c
	s_load_dwordx2 s[0:1], s[0:1], 0x40
	v_ashrrev_i32_e32 v11, 31, v10
	v_mov_b32_e32 v0, s6
	v_lshrrev_b32_e32 v4, 2, v25
	v_accvgpr_read_b32 v75, a0
	s_waitcnt lgkmcnt(0)
	s_lshl_b32 s24, s24, 7
	s_mov_b32 s0, 32
	s_mov_b32 s1, 0
	v_mul_lo_u32 v10, v10, s24
	v_mov_b32_e32 v11, 0
	s_mul_i32 s2, s1, s6
	s_mul_i32 s3, s0, s7
	s_add_i32 s4, s3, s2
	v_mad_u64_u32 v[0:1], s[2:3], s0, v0, v[10:11]
	v_or_b32_e32 v0, v0, v8
	v_lshl_or_b32 v77, v8, 1, v76
	v_mul_u32_u24_e32 v8, 40, v4
	s_waitcnt vmcnt(0)
	v_lshl_add_u32 v78, v8, 1, v77
	v_fma_f32 v8, s5, v75, v9
	v_max_f32_e32 v8, 0, v8
	s_mov_b32 s2, 0x43800000
	v_mul_u32_u24_e32 v11, 0xa0, v26
	v_fma_mixlo_f16 v10, v8, s2, 0
	v_or_b32_e32 v11, v11, v24
	v_accvgpr_read_b32 v74, a1
	v_fma_mixlo_f16 v8, v8, s2, -v10 op_sel_hi:[0,0,1]
	v_lshl_or_b32 v26, v11, 1, v76
	s_barrier
	ds_write_b16 v26, v10
	ds_write_b16 v26, v8 offset:5120
	v_fma_f32 v8, s5, v74, v9
	v_max_f32_e32 v8, 0, v8
	v_fma_mixlo_f16 v10, v8, s2, 0
	v_accvgpr_read_b32 v73, a2
	v_fma_mixlo_f16 v8, v8, s2, -v10 op_sel_hi:[0,0,1]
	ds_write_b16 v26, v10 offset:80
	ds_write_b16 v26, v8 offset:5200
	v_fma_f32 v8, s5, v73, v9
	v_max_f32_e32 v8, 0, v8
	v_fma_mixlo_f16 v10, v8, s2, 0
	v_accvgpr_read_b32 v72, a3
	v_fma_mixlo_f16 v8, v8, s2, -v10 op_sel_hi:[0,0,1]
	ds_write_b16 v26, v10 offset:160
	ds_write_b16 v26, v8 offset:5280
	v_fma_f32 v8, s5, v72, v9
	v_max_f32_e32 v8, 0, v8
	v_fma_mixlo_f16 v10, v8, s2, 0
	v_accvgpr_read_b32 v71, a4
	v_fma_mixlo_f16 v8, v8, s2, -v10 op_sel_hi:[0,0,1]
	ds_write_b16 v26, v10 offset:240
	ds_write_b16 v26, v8 offset:5360
	v_fma_f32 v8, s5, v71, v9
	v_max_f32_e32 v8, 0, v8
	v_fma_mixlo_f16 v10, v8, s2, 0
	v_accvgpr_read_b32 v70, a5
	v_fma_mixlo_f16 v8, v8, s2, -v10 op_sel_hi:[0,0,1]
	ds_write_b16 v26, v10 offset:640
	ds_write_b16 v26, v8 offset:5760
	v_fma_f32 v8, s5, v70, v9
	v_max_f32_e32 v8, 0, v8
	v_fma_mixlo_f16 v10, v8, s2, 0
	v_accvgpr_read_b32 v69, a6
	v_fma_mixlo_f16 v8, v8, s2, -v10 op_sel_hi:[0,0,1]
	ds_write_b16 v26, v10 offset:720
	ds_write_b16 v26, v8 offset:5840
	v_fma_f32 v8, s5, v69, v9
	v_max_f32_e32 v8, 0, v8
	v_fma_mixlo_f16 v10, v8, s2, 0
	v_accvgpr_read_b32 v68, a7
	v_fma_mixlo_f16 v8, v8, s2, -v10 op_sel_hi:[0,0,1]
	ds_write_b16 v26, v10 offset:800
	ds_write_b16 v26, v8 offset:5920
	v_fma_f32 v8, s5, v68, v9
	v_max_f32_e32 v8, 0, v8
	v_fma_mixlo_f16 v10, v8, s2, 0
	v_accvgpr_read_b32 v67, a8
	v_fma_mixlo_f16 v8, v8, s2, -v10 op_sel_hi:[0,0,1]
	ds_write_b16 v26, v10 offset:880
	ds_write_b16 v26, v8 offset:6000
	v_fma_f32 v8, s5, v67, v9
	v_max_f32_e32 v8, 0, v8
	v_fma_mixlo_f16 v10, v8, s2, 0
	v_accvgpr_read_b32 v66, a9
	v_fma_mixlo_f16 v8, v8, s2, -v10 op_sel_hi:[0,0,1]
	ds_write_b16 v26, v10 offset:1280
	ds_write_b16 v26, v8 offset:6400
	v_fma_f32 v8, s5, v66, v9
	v_max_f32_e32 v8, 0, v8
	v_fma_mixlo_f16 v10, v8, s2, 0
	v_accvgpr_read_b32 v65, a10
	v_fma_mixlo_f16 v8, v8, s2, -v10 op_sel_hi:[0,0,1]
	ds_write_b16 v26, v10 offset:1360
	ds_write_b16 v26, v8 offset:6480
	v_fma_f32 v8, s5, v65, v9
	v_max_f32_e32 v8, 0, v8
	v_fma_mixlo_f16 v10, v8, s2, 0
	v_accvgpr_read_b32 v64, a11
	v_fma_mixlo_f16 v8, v8, s2, -v10 op_sel_hi:[0,0,1]
	ds_write_b16 v26, v10 offset:1440
	ds_write_b16 v26, v8 offset:6560
	v_fma_f32 v8, s5, v64, v9
	v_max_f32_e32 v8, 0, v8
	v_fma_mixlo_f16 v10, v8, s2, 0
	v_accvgpr_read_b32 v63, a12
	v_fma_mixlo_f16 v8, v8, s2, -v10 op_sel_hi:[0,0,1]
	ds_write_b16 v26, v10 offset:1520
	ds_write_b16 v26, v8 offset:6640
	v_fma_f32 v8, s5, v63, v9
	v_max_f32_e32 v8, 0, v8
	v_fma_mixlo_f16 v10, v8, s2, 0
	v_accvgpr_read_b32 v62, a13
	v_fma_mixlo_f16 v8, v8, s2, -v10 op_sel_hi:[0,0,1]
	ds_write_b16 v26, v10 offset:1920
	ds_write_b16 v26, v8 offset:7040
	v_fma_f32 v8, s5, v62, v9
	v_max_f32_e32 v8, 0, v8
	v_fma_mixlo_f16 v10, v8, s2, 0
	v_accvgpr_read_b32 v61, a14
	v_fma_mixlo_f16 v8, v8, s2, -v10 op_sel_hi:[0,0,1]
	ds_write_b16 v26, v10 offset:2000
	ds_write_b16 v26, v8 offset:7120
	v_fma_f32 v8, s5, v61, v9
	v_max_f32_e32 v8, 0, v8
	v_fma_mixlo_f16 v10, v8, s2, 0
	v_accvgpr_read_b32 v60, a15
	v_fma_mixlo_f16 v8, v8, s2, -v10 op_sel_hi:[0,0,1]
	ds_write_b16 v26, v10 offset:2080
	ds_write_b16 v26, v8 offset:7200
	v_fma_f32 v8, s5, v60, v9
	v_max_f32_e32 v8, 0, v8
	v_fma_mixlo_f16 v10, v8, s2, 0
	v_accvgpr_read_b32 v59, a16
	v_fma_mixlo_f16 v8, v8, s2, -v10 op_sel_hi:[0,0,1]
	ds_write_b16 v26, v10 offset:2160
	ds_write_b16 v26, v8 offset:7280
	v_fma_f32 v8, s5, v59, v9
	v_max_f32_e32 v8, 0, v8
	v_fma_mixlo_f16 v10, v8, s2, 0
	v_accvgpr_read_b32 v58, a17
	v_fma_mixlo_f16 v8, v8, s2, -v10 op_sel_hi:[0,0,1]
	ds_write_b16 v26, v10 offset:2560
	ds_write_b16 v26, v8 offset:7680
	v_fma_f32 v8, s5, v58, v9
	v_max_f32_e32 v8, 0, v8
	v_fma_mixlo_f16 v10, v8, s2, 0
	v_accvgpr_read_b32 v57, a18
	v_fma_mixlo_f16 v8, v8, s2, -v10 op_sel_hi:[0,0,1]
	ds_write_b16 v26, v10 offset:2640
	ds_write_b16 v26, v8 offset:7760
	v_fma_f32 v8, s5, v57, v9
	v_max_f32_e32 v8, 0, v8
	v_fma_mixlo_f16 v10, v8, s2, 0
	v_accvgpr_read_b32 v56, a19
	v_fma_mixlo_f16 v8, v8, s2, -v10 op_sel_hi:[0,0,1]
	ds_write_b16 v26, v10 offset:2720
	ds_write_b16 v26, v8 offset:7840
	v_fma_f32 v8, s5, v56, v9
	v_max_f32_e32 v8, 0, v8
	v_fma_mixlo_f16 v10, v8, s2, 0
	v_accvgpr_read_b32 v55, a20
	v_fma_mixlo_f16 v8, v8, s2, -v10 op_sel_hi:[0,0,1]
	ds_write_b16 v26, v10 offset:2800
	ds_write_b16 v26, v8 offset:7920
	v_fma_f32 v8, s5, v55, v9
	v_max_f32_e32 v8, 0, v8
	v_fma_mixlo_f16 v10, v8, s2, 0
	v_accvgpr_read_b32 v54, a21
	v_fma_mixlo_f16 v8, v8, s2, -v10 op_sel_hi:[0,0,1]
	ds_write_b16 v26, v10 offset:3200
	ds_write_b16 v26, v8 offset:8320
	v_fma_f32 v8, s5, v54, v9
	v_max_f32_e32 v8, 0, v8
	v_fma_mixlo_f16 v10, v8, s2, 0
	v_accvgpr_read_b32 v53, a22
	v_fma_mixlo_f16 v8, v8, s2, -v10 op_sel_hi:[0,0,1]
	ds_write_b16 v26, v10 offset:3280
	ds_write_b16 v26, v8 offset:8400
	v_fma_f32 v8, s5, v53, v9
	v_max_f32_e32 v8, 0, v8
	v_fma_mixlo_f16 v10, v8, s2, 0
	v_accvgpr_read_b32 v52, a23
	v_fma_mixlo_f16 v8, v8, s2, -v10 op_sel_hi:[0,0,1]
	ds_write_b16 v26, v10 offset:3360
	ds_write_b16 v26, v8 offset:8480
	v_fma_f32 v8, s5, v52, v9
	v_max_f32_e32 v8, 0, v8
	v_fma_mixlo_f16 v10, v8, s2, 0
	v_accvgpr_read_b32 v51, a24
	v_fma_mixlo_f16 v8, v8, s2, -v10 op_sel_hi:[0,0,1]
	ds_write_b16 v26, v10 offset:3440
	ds_write_b16 v26, v8 offset:8560
	v_fma_f32 v8, s5, v51, v9
	v_max_f32_e32 v8, 0, v8
	v_fma_mixlo_f16 v10, v8, s2, 0
	v_accvgpr_read_b32 v50, a25
	v_fma_mixlo_f16 v8, v8, s2, -v10 op_sel_hi:[0,0,1]
	ds_write_b16 v26, v10 offset:3840
	ds_write_b16 v26, v8 offset:8960
	v_fma_f32 v8, s5, v50, v9
	v_max_f32_e32 v8, 0, v8
	v_fma_mixlo_f16 v10, v8, s2, 0
	v_accvgpr_read_b32 v49, a26
	v_fma_mixlo_f16 v8, v8, s2, -v10 op_sel_hi:[0,0,1]
	ds_write_b16 v26, v10 offset:3920
	ds_write_b16 v26, v8 offset:9040
	v_fma_f32 v8, s5, v49, v9
	v_max_f32_e32 v8, 0, v8
	v_fma_mixlo_f16 v10, v8, s2, 0
	v_accvgpr_read_b32 v48, a27
	v_fma_mixlo_f16 v8, v8, s2, -v10 op_sel_hi:[0,0,1]
	ds_write_b16 v26, v10 offset:4000
	ds_write_b16 v26, v8 offset:9120
	v_fma_f32 v8, s5, v48, v9
	v_max_f32_e32 v8, 0, v8
	v_fma_mixlo_f16 v10, v8, s2, 0
	v_accvgpr_read_b32 v47, a28
	v_fma_mixlo_f16 v8, v8, s2, -v10 op_sel_hi:[0,0,1]
	ds_write_b16 v26, v10 offset:4080
	ds_write_b16 v26, v8 offset:9200
	v_fma_f32 v8, s5, v47, v9
	v_max_f32_e32 v8, 0, v8
	v_fma_mixlo_f16 v10, v8, s2, 0
	v_accvgpr_read_b32 v46, a29
	v_fma_mixlo_f16 v8, v8, s2, -v10 op_sel_hi:[0,0,1]
	ds_write_b16 v26, v10 offset:4480
	ds_write_b16 v26, v8 offset:9600
	v_fma_f32 v8, s5, v46, v9
	v_max_f32_e32 v8, 0, v8
	v_fma_mixlo_f16 v10, v8, s2, 0
	v_accvgpr_read_b32 v45, a30
	v_fma_mixlo_f16 v8, v8, s2, -v10 op_sel_hi:[0,0,1]
	ds_write_b16 v26, v10 offset:4560
	ds_write_b16 v26, v8 offset:9680
	v_fma_f32 v8, s5, v45, v9
	v_max_f32_e32 v8, 0, v8
	v_fma_mixlo_f16 v10, v8, s2, 0
	v_accvgpr_read_b32 v44, a31
	v_fma_mixlo_f16 v8, v8, s2, -v10 op_sel_hi:[0,0,1]
	ds_write_b16 v26, v10 offset:4640
	ds_write_b16 v26, v8 offset:9760
	v_fma_f32 v8, s5, v44, v9
	v_max_f32_e32 v8, 0, v8
	v_fma_mixlo_f16 v10, v8, s2, 0
	v_fma_mixlo_f16 v8, v8, s2, -v10 op_sel_hi:[0,0,1]
	ds_write_b16 v26, v10 offset:4720
	ds_write_b16 v26, v8 offset:9840
	v_mad_u64_u32 v[10:11], s[6:7], s0, v4, 0
	v_mov_b32_e32 v8, v11
	v_add_u32_e32 v1, s4, v1
	ds_read_b128 v[44:47], v78
	ds_read_b128 v[48:51], v78 offset:5120
	v_mad_u64_u32 v[24:25], s[6:7], s1, v4, v[8:9]
	v_lshlrev_b64 v[0:1], 1, v[0:1]
	v_mov_b32_e32 v11, v24
	v_lshl_add_u64 v[2:3], s[8:9], 0, v[0:1]
	v_lshlrev_b64 v[10:11], 1, v[10:11]
	v_lshl_add_u64 v[0:1], s[10:11], 0, v[0:1]
	v_lshl_add_u64 v[24:25], v[2:3], 0, v[10:11]
	s_waitcnt lgkmcnt(1)
	global_store_dwordx4 v[24:25], v[44:47], off sc1
	v_lshl_add_u64 v[10:11], v[0:1], 0, v[10:11]
	v_or_b32_e32 v24, 16, v4
	s_waitcnt lgkmcnt(0)
	global_store_dwordx4 v[10:11], v[48:51], off sc1
	v_mul_u32_u24_e32 v8, 40, v24
	v_mad_u64_u32 v[10:11], s[6:7], s0, v24, 0
	v_lshl_add_u32 v56, v8, 1, v77
	v_mov_b32_e32 v8, v11
	ds_read_b128 v[44:47], v56
	ds_read_b128 v[48:51], v56 offset:5120
	v_mad_u64_u32 v[24:25], s[6:7], s1, v24, v[8:9]
	v_mov_b32_e32 v11, v24
	v_lshlrev_b64 v[10:11], 1, v[10:11]
	v_lshl_add_u64 v[24:25], v[2:3], 0, v[10:11]
	s_waitcnt lgkmcnt(1)
	global_store_dwordx4 v[24:25], v[44:47], off sc1
	v_lshl_add_u64 v[10:11], v[0:1], 0, v[10:11]
	v_or_b32_e32 v24, 32, v4
	s_waitcnt lgkmcnt(0)
	global_store_dwordx4 v[10:11], v[48:51], off sc1
	v_mad_u64_u32 v[10:11], s[6:7], s0, v24, 0
	ds_read_b128 v[52:55], v56 offset:1280
	ds_read_b128 v[44:47], v56 offset:2560
	v_mov_b32_e32 v8, v11
	ds_read_b128 v[48:51], v56 offset:6400
	v_mad_u64_u32 v[24:25], s[6:7], s1, v24, v[8:9]
	v_mov_b32_e32 v11, v24
	v_lshlrev_b64 v[10:11], 1, v[10:11]
	v_lshl_add_u64 v[24:25], v[2:3], 0, v[10:11]
	s_waitcnt lgkmcnt(2)
	global_store_dwordx4 v[24:25], v[52:55], off sc1
	v_lshl_add_u64 v[10:11], v[0:1], 0, v[10:11]
	v_or_b32_e32 v24, 48, v4
	ds_read_b128 v[52:55], v56 offset:7680
	s_waitcnt lgkmcnt(1)
	global_store_dwordx4 v[10:11], v[48:51], off sc1
	v_mad_u64_u32 v[10:11], s[6:7], s0, v24, 0
	v_mov_b32_e32 v8, v11
	v_mad_u64_u32 v[24:25], s[6:7], s1, v24, v[8:9]
	v_accvgpr_read_b32 v43, a32
	v_mov_b32_e32 v11, v24
	v_lshlrev_b64 v[10:11], 1, v[10:11]
	v_fma_f32 v8, s5, v43, v9
	v_lshl_add_u64 v[24:25], v[2:3], 0, v[10:11]
	v_lshl_add_u64 v[10:11], v[0:1], 0, v[10:11]
	v_max_f32_e32 v8, 0, v8
	s_waitcnt lgkmcnt(0)
	global_store_dwordx4 v[10:11], v[52:55], off sc1
	v_fma_mixlo_f16 v10, v8, s2, 0
	v_accvgpr_read_b32 v42, a33
	v_fma_mixlo_f16 v8, v8, s2, -v10 op_sel_hi:[0,0,1]
	global_store_dwordx4 v[24:25], v[44:47], off sc1
	ds_write_b16 v26, v10
	ds_write_b16 v26, v8 offset:5120
	v_fma_f32 v8, s5, v42, v9
	v_max_f32_e32 v8, 0, v8
	v_fma_mixlo_f16 v10, v8, s2, 0
	v_accvgpr_read_b32 v41, a34
	v_fma_mixlo_f16 v8, v8, s2, -v10 op_sel_hi:[0,0,1]
	ds_write_b16 v26, v10 offset:80
	ds_write_b16 v26, v8 offset:5200
	v_fma_f32 v8, s5, v41, v9
	v_max_f32_e32 v8, 0, v8
	v_fma_mixlo_f16 v10, v8, s2, 0
	v_accvgpr_read_b32 v40, a35
	v_fma_mixlo_f16 v8, v8, s2, -v10 op_sel_hi:[0,0,1]
	ds_write_b16 v26, v10 offset:160
	ds_write_b16 v26, v8 offset:5280
	v_fma_f32 v8, s5, v40, v9
	v_max_f32_e32 v8, 0, v8
	v_fma_mixlo_f16 v10, v8, s2, 0
	v_accvgpr_read_b32 v39, a36
	v_fma_mixlo_f16 v8, v8, s2, -v10 op_sel_hi:[0,0,1]
	ds_write_b16 v26, v10 offset:240
	ds_write_b16 v26, v8 offset:5360
	v_fma_f32 v8, s5, v39, v9
	v_max_f32_e32 v8, 0, v8
	v_fma_mixlo_f16 v10, v8, s2, 0
	v_accvgpr_read_b32 v38, a37
	v_fma_mixlo_f16 v8, v8, s2, -v10 op_sel_hi:[0,0,1]
	ds_write_b16 v26, v10 offset:640
	ds_write_b16 v26, v8 offset:5760
	v_fma_f32 v8, s5, v38, v9
	v_max_f32_e32 v8, 0, v8
	v_fma_mixlo_f16 v10, v8, s2, 0
	v_accvgpr_read_b32 v37, a38
	v_fma_mixlo_f16 v8, v8, s2, -v10 op_sel_hi:[0,0,1]
	ds_write_b16 v26, v10 offset:720
	ds_write_b16 v26, v8 offset:5840
	v_fma_f32 v8, s5, v37, v9
	v_max_f32_e32 v8, 0, v8
	v_fma_mixlo_f16 v10, v8, s2, 0
	v_accvgpr_read_b32 v36, a39
	v_fma_mixlo_f16 v8, v8, s2, -v10 op_sel_hi:[0,0,1]
	ds_write_b16 v26, v10 offset:800
	ds_write_b16 v26, v8 offset:5920
	v_fma_f32 v8, s5, v36, v9
	v_max_f32_e32 v8, 0, v8
	v_fma_mixlo_f16 v10, v8, s2, 0
	v_accvgpr_read_b32 v35, a40
	v_fma_mixlo_f16 v8, v8, s2, -v10 op_sel_hi:[0,0,1]
	ds_write_b16 v26, v10 offset:880
	ds_write_b16 v26, v8 offset:6000
	v_fma_f32 v8, s5, v35, v9
	v_max_f32_e32 v8, 0, v8
	v_fma_mixlo_f16 v10, v8, s2, 0
	v_accvgpr_read_b32 v34, a41
	v_fma_mixlo_f16 v8, v8, s2, -v10 op_sel_hi:[0,0,1]
	ds_write_b16 v26, v10 offset:1280
	ds_write_b16 v26, v8 offset:6400
	v_fma_f32 v8, s5, v34, v9
	v_max_f32_e32 v8, 0, v8
	v_fma_mixlo_f16 v10, v8, s2, 0
	v_accvgpr_read_b32 v33, a42
	v_fma_mixlo_f16 v8, v8, s2, -v10 op_sel_hi:[0,0,1]
	ds_write_b16 v26, v10 offset:1360
	ds_write_b16 v26, v8 offset:6480
	v_fma_f32 v8, s5, v33, v9
	v_max_f32_e32 v8, 0, v8
	v_fma_mixlo_f16 v10, v8, s2, 0
	v_accvgpr_read_b32 v32, a43
	v_fma_mixlo_f16 v8, v8, s2, -v10 op_sel_hi:[0,0,1]
	ds_write_b16 v26, v10 offset:1440
	ds_write_b16 v26, v8 offset:6560
	v_fma_f32 v8, s5, v32, v9
	v_max_f32_e32 v8, 0, v8
	v_fma_mixlo_f16 v10, v8, s2, 0
	v_accvgpr_read_b32 v31, a44
	v_fma_mixlo_f16 v8, v8, s2, -v10 op_sel_hi:[0,0,1]
	ds_write_b16 v26, v10 offset:1520
	ds_write_b16 v26, v8 offset:6640
	v_fma_f32 v8, s5, v31, v9
	v_max_f32_e32 v8, 0, v8
	v_fma_mixlo_f16 v10, v8, s2, 0
	v_accvgpr_read_b32 v30, a45
	v_fma_mixlo_f16 v8, v8, s2, -v10 op_sel_hi:[0,0,1]
	ds_write_b16 v26, v10 offset:1920
	ds_write_b16 v26, v8 offset:7040
	v_fma_f32 v8, s5, v30, v9
	v_max_f32_e32 v8, 0, v8
	v_fma_mixlo_f16 v10, v8, s2, 0
	v_accvgpr_read_b32 v29, a46
	v_fma_mixlo_f16 v8, v8, s2, -v10 op_sel_hi:[0,0,1]
	ds_write_b16 v26, v10 offset:2000
	ds_write_b16 v26, v8 offset:7120
	v_fma_f32 v8, s5, v29, v9
	v_max_f32_e32 v8, 0, v8
	v_fma_mixlo_f16 v10, v8, s2, 0
	v_accvgpr_read_b32 v28, a47
	v_fma_mixlo_f16 v8, v8, s2, -v10 op_sel_hi:[0,0,1]
	ds_write_b16 v26, v10 offset:2080
	ds_write_b16 v26, v8 offset:7200
	v_fma_f32 v8, s5, v28, v9
	v_max_f32_e32 v8, 0, v8
	v_fma_mixlo_f16 v10, v8, s2, 0
	v_accvgpr_read_b32 v27, a48
	v_fma_mixlo_f16 v8, v8, s2, -v10 op_sel_hi:[0,0,1]
	ds_write_b16 v26, v10 offset:2160
	ds_write_b16 v26, v8 offset:7280
	v_fma_f32 v8, s5, v27, v9
	v_max_f32_e32 v8, 0, v8
	v_fma_mixlo_f16 v10, v8, s2, 0
	v_accvgpr_read_b32 v23, a49
	v_fma_mixlo_f16 v8, v8, s2, -v10 op_sel_hi:[0,0,1]
	ds_write_b16 v26, v10 offset:2560
	ds_write_b16 v26, v8 offset:7680
	v_fma_f32 v8, s5, v23, v9
	v_max_f32_e32 v8, 0, v8
	v_fma_mixlo_f16 v10, v8, s2, 0
	v_accvgpr_read_b32 v22, a50
	v_fma_mixlo_f16 v8, v8, s2, -v10 op_sel_hi:[0,0,1]
	ds_write_b16 v26, v10 offset:2640
	ds_write_b16 v26, v8 offset:7760
	v_fma_f32 v8, s5, v22, v9
	v_max_f32_e32 v8, 0, v8
	v_fma_mixlo_f16 v10, v8, s2, 0
	v_accvgpr_read_b32 v21, a51
	v_fma_mixlo_f16 v8, v8, s2, -v10 op_sel_hi:[0,0,1]
	ds_write_b16 v26, v10 offset:2720
	ds_write_b16 v26, v8 offset:7840
	v_fma_f32 v8, s5, v21, v9
	v_max_f32_e32 v8, 0, v8
	v_fma_mixlo_f16 v10, v8, s2, 0
	v_accvgpr_read_b32 v20, a52
	v_fma_mixlo_f16 v8, v8, s2, -v10 op_sel_hi:[0,0,1]
	ds_write_b16 v26, v10 offset:2800
	ds_write_b16 v26, v8 offset:7920
	v_fma_f32 v8, s5, v20, v9
	v_max_f32_e32 v8, 0, v8
	v_fma_mixlo_f16 v10, v8, s2, 0
	v_accvgpr_read_b32 v19, a53
	v_fma_mixlo_f16 v8, v8, s2, -v10 op_sel_hi:[0,0,1]
	ds_write_b16 v26, v10 offset:3200
	ds_write_b16 v26, v8 offset:8320
	v_fma_f32 v8, s5, v19, v9
	v_max_f32_e32 v8, 0, v8
	v_fma_mixlo_f16 v10, v8, s2, 0
	v_accvgpr_read_b32 v18, a54
	v_fma_mixlo_f16 v8, v8, s2, -v10 op_sel_hi:[0,0,1]
	ds_write_b16 v26, v10 offset:3280
	ds_write_b16 v26, v8 offset:8400
	v_fma_f32 v8, s5, v18, v9
	v_max_f32_e32 v8, 0, v8
	v_fma_mixlo_f16 v10, v8, s2, 0
	v_accvgpr_read_b32 v17, a55
	v_fma_mixlo_f16 v8, v8, s2, -v10 op_sel_hi:[0,0,1]
	ds_write_b16 v26, v10 offset:3360
	ds_write_b16 v26, v8 offset:8480
	v_fma_f32 v8, s5, v17, v9
	v_max_f32_e32 v8, 0, v8
	v_fma_mixlo_f16 v10, v8, s2, 0
	v_accvgpr_read_b32 v16, a56
	v_fma_mixlo_f16 v8, v8, s2, -v10 op_sel_hi:[0,0,1]
	ds_write_b16 v26, v10 offset:3440
	ds_write_b16 v26, v8 offset:8560
	v_fma_f32 v8, s5, v16, v9
	v_max_f32_e32 v8, 0, v8
	v_fma_mixlo_f16 v10, v8, s2, 0
	v_accvgpr_read_b32 v15, a57
	v_fma_mixlo_f16 v8, v8, s2, -v10 op_sel_hi:[0,0,1]
	ds_write_b16 v26, v10 offset:3840
	ds_write_b16 v26, v8 offset:8960
	v_fma_f32 v8, s5, v15, v9
	v_max_f32_e32 v8, 0, v8
	v_fma_mixlo_f16 v10, v8, s2, 0
	v_accvgpr_read_b32 v14, a58
	v_fma_mixlo_f16 v8, v8, s2, -v10 op_sel_hi:[0,0,1]
	ds_write_b16 v26, v10 offset:3920
	ds_write_b16 v26, v8 offset:9040
	v_fma_f32 v8, s5, v14, v9
	v_max_f32_e32 v8, 0, v8
	v_fma_mixlo_f16 v10, v8, s2, 0
	v_accvgpr_read_b32 v13, a59
	v_fma_mixlo_f16 v8, v8, s2, -v10 op_sel_hi:[0,0,1]
	ds_write_b16 v26, v10 offset:4000
	ds_write_b16 v26, v8 offset:9120
	v_fma_f32 v8, s5, v13, v9
	v_max_f32_e32 v8, 0, v8
	v_fma_mixlo_f16 v10, v8, s2, 0
	v_accvgpr_read_b32 v12, a60
	v_fma_mixlo_f16 v8, v8, s2, -v10 op_sel_hi:[0,0,1]
	ds_write_b16 v26, v10 offset:4080
	ds_write_b16 v26, v8 offset:9200
	v_fma_f32 v8, s5, v12, v9
	v_accvgpr_read_b32 v7, a61
	v_max_f32_e32 v8, 0, v8
	v_fma_mixlo_f16 v10, v8, s2, 0
	v_fma_f32 v7, s5, v7, v9
	v_accvgpr_read_b32 v6, a62
	v_fma_mixlo_f16 v8, v8, s2, -v10 op_sel_hi:[0,0,1]
	v_max_f32_e32 v7, 0, v7
	ds_write_b16 v26, v10 offset:4480
	ds_write_b16 v26, v8 offset:9600
	v_fma_mixlo_f16 v8, v7, s2, 0
	v_fma_f32 v6, s5, v6, v9
	v_accvgpr_read_b32 v5, a63
	v_fma_mixlo_f16 v7, v7, s2, -v8 op_sel_hi:[0,0,1]
	v_max_f32_e32 v6, 0, v6
	ds_write_b16 v26, v8 offset:4560
	ds_write_b16 v26, v7 offset:9680
	v_fma_mixlo_f16 v7, v6, s2, 0
	v_fmac_f32_e32 v9, s5, v5
	v_fma_mixlo_f16 v6, v6, s2, -v7 op_sel_hi:[0,0,1]
	v_max_f32_e32 v5, 0, v9
	ds_write_b16 v26, v7 offset:4640
	ds_write_b16 v26, v6 offset:9760
	v_fma_mixlo_f16 v6, v5, s2, 0
	v_fma_mixlo_f16 v5, v5, s2, -v6 op_sel_hi:[0,0,1]
	ds_write_b16 v26, v6 offset:4720
	ds_write_b16 v26, v5 offset:9840
	v_or_b32_e32 v5, 64, v4
	v_mad_u64_u32 v[14:15], s[2:3], s0, v5, 0
	v_mov_b32_e32 v16, v15
	ds_read_b128 v[6:9], v78
	ds_read_b128 v[10:13], v78 offset:5120
	v_mad_u64_u32 v[16:17], s[2:3], s1, v5, v[16:17]
	v_mov_b32_e32 v15, v16
	v_lshlrev_b64 v[14:15], 1, v[14:15]
	v_lshl_add_u64 v[16:17], v[2:3], 0, v[14:15]
	s_waitcnt lgkmcnt(1)
	global_store_dwordx4 v[16:17], v[6:9], off sc1
	v_or_b32_e32 v5, 0x50, v4
	s_nop 0
	v_lshl_add_u64 v[6:7], v[0:1], 0, v[14:15]
	s_waitcnt lgkmcnt(0)
	global_store_dwordx4 v[6:7], v[10:13], off sc1
	v_mad_u64_u32 v[14:15], s[2:3], s0, v5, 0
	ds_read_b128 v[6:9], v56
	ds_read_b128 v[10:13], v56 offset:5120
	v_mov_b32_e32 v16, v15
	v_mad_u64_u32 v[16:17], s[2:3], s1, v5, v[16:17]
	v_mov_b32_e32 v15, v16
	v_lshlrev_b64 v[18:19], 1, v[14:15]
	v_lshl_add_u64 v[20:21], v[2:3], 0, v[18:19]
	v_lshl_add_u64 v[18:19], v[0:1], 0, v[18:19]
	v_or_b32_e32 v5, 0x60, v4
	s_waitcnt lgkmcnt(0)
	global_store_dwordx4 v[18:19], v[10:13], off sc1
	v_mad_u64_u32 v[18:19], s[2:3], s0, v5, 0
	ds_read_b128 v[14:17], v56 offset:1280
	global_store_dwordx4 v[20:21], v[6:9], off sc1
	ds_read_b128 v[10:13], v56 offset:6400
	v_mov_b32_e32 v20, v19
	v_mad_u64_u32 v[20:21], s[2:3], s1, v5, v[20:21]
	v_mov_b32_e32 v19, v20
	v_lshlrev_b64 v[18:19], 1, v[18:19]
	v_lshl_add_u64 v[20:21], v[2:3], 0, v[18:19]
	v_lshl_add_u64 v[18:19], v[0:1], 0, v[18:19]
	ds_read_b128 v[6:9], v56 offset:2560
	s_waitcnt lgkmcnt(2)
	global_store_dwordx4 v[20:21], v[14:17], off sc1
	ds_read_b128 v[14:17], v56 offset:7680
	s_waitcnt lgkmcnt(2)
	global_store_dwordx4 v[18:19], v[10:13], off sc1
	s_nop 1
	v_or_b32_e32 v11, 0x70, v4
	v_mad_u64_u32 v[4:5], s[2:3], s0, v11, 0
	v_mov_b32_e32 v10, v5
	v_mad_u64_u32 v[10:11], s[0:1], s1, v11, v[10:11]
	v_mov_b32_e32 v5, v10
	v_lshlrev_b64 v[4:5], 1, v[4:5]
	v_lshl_add_u64 v[2:3], v[2:3], 0, v[4:5]
	v_lshl_add_u64 v[0:1], v[0:1], 0, v[4:5]
	s_waitcnt lgkmcnt(1)
	global_store_dwordx4 v[2:3], v[6:9], off sc1
	s_waitcnt lgkmcnt(0)
	global_store_dwordx4 v[0:1], v[14:17], off sc1
	s_endpgm
	s_endpgm
	s_endpgm
	s_endpgm
	s_endpgm
	s_endpgm
	s_endpgm
	s_endpgm
	s_endpgm
	s_endpgm
	s_endpgm
	s_endpgm
	s_endpgm
	s_endpgm
	s_endpgm
	s_endpgm
	s_endpgm
	s_endpgm
	s_endpgm
	s_endpgm
	s_endpgm
	s_endpgm
	s_endpgm
	s_endpgm
	s_endpgm
	s_endpgm
	s_endpgm
	s_endpgm
	s_endpgm
	s_endpgm
	s_endpgm
	s_endpgm
	s_endpgm
	s_endpgm
	s_endpgm
	s_endpgm
	s_endpgm
	s_endpgm
	s_endpgm
	s_endpgm
	s_endpgm
	s_endpgm
	s_endpgm
	s_endpgm
	s_endpgm
